# norm row loops: first row's gate pair and expert-row indices requested at the loop top (one dwordx2 each) instead of behind the residual-row loads: gather loads start two round trips earlier
# baseline (speedup 1.0000x reference)
; #define GAS __attribute__((address_space(1)))
; __device__ __forceinline__ float bflo(unsigned w) { return __uint_as_float(w << 16); }
; __device__ __forceinline__ float bfhi(unsigned w) { return __uint_as_float(w & 0xffff0000u); }
; template <int MODE, bool W8 = false>
; __device__ __forceinline__ void norm_rows(const Ctx& C, const void* src, bf16* xdst, const unsigned char* YS8, const int* srow, const float* gate, const float* gain, bf16* XN, float* outf, unsigned char* XN8 = nullptr) {
;     ...
;     for (int m0 = C.gw; m0 < T; m0 += NR * C.NGW) {
;         f32x4 v[NR][8]; unsigned ya[NR][8], yb[NR][8]; float h0[NR], h1[NR];
; #pragma unroll
;         for (int q = 0; q < NR; ++q) { const int m = m0 + q * C.NGW;
;             if (MODE == 0) { const GAS f32x4* xr = (const GAS f32x4*)((const float*)src + (size_t)m * DM) + C.lane;
; #pragma unroll
;                 for (int j = 0; j < 8; ++j) v[q][j] = xr[64 * j]; }
;             else { const GAS v2u* xr = (const GAS v2u*)((const bf16*)src + (size_t)m * DM) + C.lane;
; #pragma unroll
;                 for (int j = 0; j < 8; ++j) { const v2u t_ = xr[64 * j]; v[q][j] = (f32x4){bflo(t_.x), bfhi(t_.x), bflo(t_.y), bfhi(t_.y)}; } }
;             if (MODE >= 1) {
;                 h0[q] = gate[2 * m] * (1.0f / SY); h1[q] = gate[2 * m + 1] * (1.0f / SY);
;                 const GAS unsigned* y0 = (const GAS unsigned*)(YS8 + (size_t)srow[2 * m] * DM) + C.lane; const GAS unsigned* y1 = (const GAS unsigned*)(YS8 + (size_t)srow[2 * m + 1] * DM) + C.lane;
; #pragma unroll
;                 for (int j = 0; j < 8; ++j) { ya[q][j] = y0[64 * j]; yb[q][j] = y1[64 * j]; } } }
; #pragma unroll
;         for (int q = 0; q < NR; ++q) { const int m = m0 + q * C.NGW;
;             if (MODE >= 1) {
; #pragma unroll
;                 for (int j = 0; j < 8; ++j) { const unsigned a = ya[q][j], b = yb[q][j];
;                     const f32x2_m a01 = __builtin_amdgcn_cvt_pk_f32_fp8((int)a, false), a23 = __builtin_amdgcn_cvt_pk_f32_fp8((int)a, true), b01 = __builtin_amdgcn_cvt_pk_f32_fp8((int)b, false), b23 = __builtin_amdgcn_cvt_pk_f32_fp8((int)b, true);
;                     v[q][j].x += h0[q] * a01.x + h1[q] * b01.x; v[q][j].y += h0[q] * a01.y + h1[q] * b01.y; v[q][j].z += h0[q] * a23.x + h1[q] * b23.x; v[q][j].w += h0[q] * a23.y + h1[q] * b23.y; } }
.LBB0_1321:
	s_ashr_i32 s11, s10, 31
	s_lshl_b64 s[2:3], s[10:11], 2
	s_add_u32 s28, s24, s2
	s_addc_u32 s29, s25, s3
	global_load_dwordx2 v[192:193], v2, s[28:29]
	s_add_u32 s2, s22, s2
	s_addc_u32 s3, s23, s3
	global_load_dwordx2 v[194:195], v2, s[2:3]
	s_ashr_i32 s11, s10, 31
	v_lshl_add_u64 v[4:5], s[16:17], 0, v[22:23]
	s_lshl_b64 s[2:3], s[10:11], 2
	v_add_co_u32_e32 v4, vcc, 0x4b800000, v4
	s_add_u32 s28, s24, s2
	s_nop 0
	v_addc_co_u32_e32 v5, vcc, 0, v5, vcc
	s_addc_u32 s29, s25, s3
	global_load_dwordx2 v[58:59], v[4:5], off
	global_load_dwordx2 v[52:53], v[4:5], off offset:512
	global_load_dwordx2 v[50:51], v[4:5], off offset:1024
	global_load_dwordx2 v[48:49], v[4:5], off offset:1536
	global_load_dwordx2 v[44:45], v[4:5], off offset:2048
	global_load_dwordx2 v[46:47], v[4:5], off offset:2560
	global_load_dwordx2 v[6:7], v[4:5], off offset:3072
	s_nop 0
	global_load_dwordx2 v[4:5], v[4:5], off offset:3584
	s_waitcnt vmcnt(7)
	v_lshlrev_b32_e32 v66, 16, v58
	s_add_i32 s28, s10, 1
	s_ashr_i32 s29, s28, 31
	s_add_u32 s2, s22, s2
	s_addc_u32 s3, s23, s3
	v_and_b32_e32 v67, 0xffff0000, v58
	v_lshlrev_b32_e32 v58, 16, v59
	v_and_b32_e32 v59, 0xffff0000, v59
	s_waitcnt vmcnt(1)
	v_and_b32_e32 v99, 0xffff0000, v6
	s_waitcnt vmcnt(0)
	v_mul_f32_e32 v54, 0x3d800000, v192
	v_mov_b32_e32 v24, v194
	s_lshl_b64 s[2:3], s[28:29], 2
	s_add_u32 s2, s22, s2
	s_addc_u32 s3, s23, s3
	v_mov_b32_e32 v28, v195
	v_mul_f32_e32 v76, 0x3d800000, v193
	s_add_i32 s2, s10, 0x1000
	s_ashr_i32 s3, s2, 31
	s_lshl_b64 s[2:3], s[2:3], 2
	s_add_u32 s28, s24, s2
	s_addc_u32 s29, s25, s3
	s_waitcnt vmcnt(1)
	v_ashrrev_i32_e32 v25, 31, v24
	v_lshlrev_b64 v[24:25], 11, v[24:25]
	v_lshl_add_u64 v[24:25], v[20:21], 0, v[24:25]
	s_waitcnt vmcnt(0)
	v_ashrrev_i32_e32 v29, 31, v28
	v_lshlrev_b64 v[28:29], 11, v[28:29]
	v_lshl_add_u64 v[28:29], v[20:21], 0, v[28:29]
	global_load_dword v55, v[24:25], off
	global_load_dword v64, v[28:29], off
	global_load_dword v68, v[24:25], off offset:256
	global_load_dword v69, v[28:29], off offset:256
	global_load_dword v70, v[24:25], off offset:512
	global_load_dword v71, v[28:29], off offset:512
	global_load_dword v72, v[24:25], off offset:768
	global_load_dword v73, v[28:29], off offset:768
	global_load_dword v74, v[24:25], off offset:1024
	global_load_dword v75, v[28:29], off offset:1024
	global_load_dword v78, v[24:25], off offset:1280
	global_load_dword v79, v[28:29], off offset:1280
	global_load_dword v97, v[24:25], off offset:1536
	global_load_dword v98, v[28:29], off offset:1536
	global_load_dword v100, v[24:25], off offset:1792
	global_load_dword v101, v[28:29], off offset:1792
	v_lshl_add_u64 v[24:25], s[18:19], 0, v[22:23]
	v_add_co_u32_e32 v24, vcc, s34, v24
	s_waitcnt vmcnt(14)
	v_cvt_pk_f32_fp8_e32 v[62:63], v64
	v_addc_co_u32_e32 v25, vcc, 0, v25, vcc
	global_load_dwordx2 v[42:43], v[24:25], off
	global_load_dwordx2 v[40:41], v[24:25], off offset:512
	global_load_dwordx2 v[38:39], v[24:25], off offset:1024
	global_load_dwordx2 v[36:37], v[24:25], off offset:1536
	global_load_dwordx2 v[34:35], v[24:25], off offset:2048
	global_load_dwordx2 v[32:33], v[24:25], off offset:2560
	global_load_dwordx2 v[30:31], v[24:25], off offset:3072
	s_nop 0
	global_load_dwordx2 v[24:25], v[24:25], off offset:3584
	v_cvt_pk_f32_fp8_sdwa v[64:65], v64 src0_sel:WORD_1
	global_load_dwordx2 v[28:29], v2, s[28:29]
	s_add_i32 s28, s10, 0x1001
	s_ashr_i32 s29, s28, 31
	s_add_u32 s2, s22, s2
	s_addc_u32 s3, s23, s3
	global_load_dword v56, v2, s[2:3]
	s_lshl_b64 s[2:3], s[28:29], 2
	s_add_u32 s2, s22, s2
	s_addc_u32 s3, s23, s3
	global_load_dword v60, v2, s[2:3]
	v_pk_mul_f32 v[62:63], v[76:77], v[62:63] op_sel_hi:[0,1]
	s_addk_i32 s26, 0x1000
	s_addk_i32 s10, 0x2000
	s_waitcnt vmcnt(2)
	v_mul_f32_e32 v26, 0x3d800000, v28
	v_mul_f32_e32 v28, 0x3d800000, v29
	s_waitcnt vmcnt(1)
	v_ashrrev_i32_e32 v57, 31, v56
	v_lshlrev_b64 v[56:57], 11, v[56:57]
	v_lshl_add_u64 v[56:57], v[20:21], 0, v[56:57]
	s_waitcnt vmcnt(0)
	v_ashrrev_i32_e32 v61, 31, v60
	v_lshlrev_b64 v[60:61], 11, v[60:61]
	v_lshl_add_u64 v[60:61], v[20:21], 0, v[60:61]
	global_load_dword v96, v[56:57], off
	global_load_dword v95, v[60:61], off
	global_load_dword v94, v[56:57], off offset:256
	global_load_dword v93, v[60:61], off offset:256
	global_load_dword v92, v[56:57], off offset:512
	global_load_dword v91, v[60:61], off offset:512
	global_load_dword v90, v[56:57], off offset:768
	global_load_dword v89, v[60:61], off offset:768
	global_load_dword v88, v[56:57], off offset:1024
	global_load_dword v87, v[60:61], off offset:1024
	global_load_dword v86, v[56:57], off offset:1280
	global_load_dword v85, v[60:61], off offset:1280
	global_load_dword v84, v[56:57], off offset:1536
	global_load_dword v83, v[60:61], off offset:1536
	global_load_dword v29, v[56:57], off offset:1792
	global_load_dword v17, v[60:61], off offset:1792
	v_cvt_pk_f32_fp8_e32 v[56:57], v55
	v_cvt_pk_f32_fp8_sdwa v[60:61], v55 src0_sel:WORD_1
	v_pk_fma_f32 v[56:57], v[54:55], v[56:57], v[62:63] op_sel_hi:[0,1,1]
	v_pk_mul_f32 v[62:63], v[76:77], v[64:65] op_sel_hi:[0,1]
	v_pk_fma_f32 v[60:61], v[54:55], v[60:61], v[62:63] op_sel_hi:[0,1,1]
	v_cvt_pk_f32_fp8_e32 v[64:65], v69
	v_pk_add_f32 v[56:57], v[56:57], v[66:67]
	v_pk_add_f32 v[62:63], v[60:61], v[58:59]
	v_cvt_pk_f32_fp8_e32 v[58:59], v68
	v_cvt_pk_f32_fp8_sdwa v[66:67], v69 src0_sel:WORD_1
	v_cvt_pk_f32_fp8_sdwa v[60:61], v68 src0_sel:WORD_1
	v_pk_mul_f32 v[64:65], v[76:77], v[64:65] op_sel_hi:[0,1]
	v_pk_fma_f32 v[58:59], v[54:55], v[58:59], v[64:65] op_sel_hi:[0,1,1]
	v_pk_mul_f32 v[64:65], v[76:77], v[66:67] op_sel_hi:[0,1]
	v_lshlrev_b32_e32 v68, 16, v52
; template <int MODE, bool W8 = false>
; __device__ __forceinline__ void norm_rows(const Ctx& C, const void* src, bf16* xdst, const unsigned char* YS8, const int* srow, const float* gate, const float* gain, bf16* XN, float* outf, unsigned char* XN8 = nullptr) {
;     ...
;                 for (int j = 0; j < 8; ++j) { const unsigned a = ya[q][j], b = yb[q][j];
;                     const f32x2_m a01 = __builtin_amdgcn_cvt_pk_f32_fp8((int)a, false), a23 = __builtin_amdgcn_cvt_pk_f32_fp8((int)a, true), b01 = __builtin_amdgcn_cvt_pk_f32_fp8((int)b, false), b23 = __builtin_amdgcn_cvt_pk_f32_fp8((int)b, true);
;                     v[q][j].x += h0[q] * a01.x + h1[q] * b01.x; v[q][j].y += h0[q] * a01.y + h1[q] * b01.y; v[q][j].z += h0[q] * a23.x + h1[q] * b23.x; v[q][j].w += h0[q] * a23.y + h1[q] * b23.y; } }
;             float ss = 0.f;
; #pragma unroll
;             for (int j = 0; j < 8; ++j) ss += (v[q][j].x * v[q][j].x + v[q][j].y * v[q][j].y) + (v[q][j].z * v[q][j].z + v[q][j].w * v[q][j].w);
	v_and_b32_e32 v69, 0xffff0000, v52
	v_lshlrev_b32_e32 v52, 16, v53
	v_and_b32_e32 v53, 0xffff0000, v53
	v_pk_fma_f32 v[60:61], v[54:55], v[60:61], v[64:65] op_sel_hi:[0,1,1]
	v_pk_add_f32 v[66:67], v[60:61], v[52:53]
	v_cvt_pk_f32_fp8_e32 v[60:61], v71
	v_cvt_pk_f32_fp8_e32 v[52:53], v70
	v_pk_add_f32 v[58:59], v[58:59], v[68:69]
	v_cvt_pk_f32_fp8_sdwa v[68:69], v71 src0_sel:WORD_1
	v_cvt_pk_f32_fp8_sdwa v[64:65], v70 src0_sel:WORD_1
	v_pk_mul_f32 v[60:61], v[76:77], v[60:61] op_sel_hi:[0,1]
	v_lshlrev_b32_e32 v70, 16, v50
	v_and_b32_e32 v71, 0xffff0000, v50
	v_pk_fma_f32 v[52:53], v[54:55], v[52:53], v[60:61] op_sel_hi:[0,1,1]
	v_pk_add_f32 v[60:61], v[52:53], v[70:71]
	v_pk_mul_f32 v[52:53], v[76:77], v[68:69] op_sel_hi:[0,1]
	v_lshlrev_b32_e32 v50, 16, v51
	v_and_b32_e32 v51, 0xffff0000, v51
	v_pk_fma_f32 v[52:53], v[54:55], v[64:65], v[52:53] op_sel_hi:[0,1,1]
	v_cvt_pk_f32_fp8_e32 v[64:65], v73
	v_pk_add_f32 v[70:71], v[52:53], v[50:51]
	v_cvt_pk_f32_fp8_e32 v[50:51], v72
	v_cvt_pk_f32_fp8_sdwa v[68:69], v73 src0_sel:WORD_1
	v_cvt_pk_f32_fp8_sdwa v[52:53], v72 src0_sel:WORD_1
	v_pk_mul_f32 v[64:65], v[76:77], v[64:65] op_sel_hi:[0,1]
	v_lshlrev_b32_e32 v72, 16, v48
	v_and_b32_e32 v73, 0xffff0000, v48
	v_pk_fma_f32 v[50:51], v[54:55], v[50:51], v[64:65] op_sel_hi:[0,1,1]
	v_pk_add_f32 v[64:65], v[50:51], v[72:73]
	v_pk_mul_f32 v[50:51], v[76:77], v[68:69] op_sel_hi:[0,1]
	v_lshlrev_b32_e32 v48, 16, v49
	v_and_b32_e32 v49, 0xffff0000, v49
	v_pk_fma_f32 v[50:51], v[54:55], v[52:53], v[50:51] op_sel_hi:[0,1,1]
	v_cvt_pk_f32_fp8_e32 v[52:53], v75
	v_pk_add_f32 v[72:73], v[50:51], v[48:49]
	v_cvt_pk_f32_fp8_e32 v[48:49], v74
	v_cvt_pk_f32_fp8_sdwa v[50:51], v74 src0_sel:WORD_1
	v_cvt_pk_f32_fp8_sdwa v[74:75], v75 src0_sel:WORD_1
	v_pk_mul_f32 v[52:53], v[76:77], v[52:53] op_sel_hi:[0,1]
	v_lshlrev_b32_e32 v68, 16, v44
	v_and_b32_e32 v69, 0xffff0000, v44
	v_pk_fma_f32 v[48:49], v[54:55], v[48:49], v[52:53] op_sel_hi:[0,1,1]
	v_pk_add_f32 v[68:69], v[48:49], v[68:69]
	v_pk_mul_f32 v[48:49], v[76:77], v[74:75] op_sel_hi:[0,1]
	v_lshlrev_b32_e32 v44, 16, v45
	v_and_b32_e32 v45, 0xffff0000, v45
	v_pk_fma_f32 v[48:49], v[54:55], v[50:51], v[48:49] op_sel_hi:[0,1,1]
	v_cvt_pk_f32_fp8_e32 v[50:51], v79
	v_pk_add_f32 v[74:75], v[48:49], v[44:45]
	v_cvt_pk_f32_fp8_e32 v[44:45], v78
	v_cvt_pk_f32_fp8_sdwa v[52:53], v79 src0_sel:WORD_1
	v_cvt_pk_f32_fp8_sdwa v[48:49], v78 src0_sel:WORD_1
	v_pk_mul_f32 v[50:51], v[76:77], v[50:51] op_sel_hi:[0,1]
	v_pk_fma_f32 v[44:45], v[54:55], v[44:45], v[50:51] op_sel_hi:[0,1,1]
	v_pk_mul_f32 v[50:51], v[76:77], v[52:53] op_sel_hi:[0,1]
	v_lshlrev_b32_e32 v78, 16, v46
	v_and_b32_e32 v79, 0xffff0000, v46
	v_lshlrev_b32_e32 v46, 16, v47
	v_and_b32_e32 v47, 0xffff0000, v47
	v_pk_fma_f32 v[48:49], v[54:55], v[48:49], v[50:51] op_sel_hi:[0,1,1]
	v_cvt_pk_f32_fp8_e32 v[52:53], v98
	v_pk_add_f32 v[44:45], v[44:45], v[78:79]
	v_pk_add_f32 v[46:47], v[48:49], v[46:47]
	v_cvt_pk_f32_fp8_e32 v[48:49], v97
	v_cvt_pk_f32_fp8_sdwa v[78:79], v98 src0_sel:WORD_1
	v_cvt_pk_f32_fp8_sdwa v[50:51], v97 src0_sel:WORD_1
	v_pk_mul_f32 v[52:53], v[76:77], v[52:53] op_sel_hi:[0,1]
	v_pk_fma_f32 v[48:49], v[54:55], v[48:49], v[52:53] op_sel_hi:[0,1,1]
	v_pk_mul_f32 v[52:53], v[76:77], v[78:79] op_sel_hi:[0,1]
	v_lshlrev_b32_e32 v98, 16, v6
	v_lshlrev_b32_e32 v6, 16, v7
	v_and_b32_e32 v7, 0xffff0000, v7
	v_pk_fma_f32 v[50:51], v[54:55], v[50:51], v[52:53] op_sel_hi:[0,1,1]
	v_cvt_pk_f32_fp8_e32 v[52:53], v101
	v_pk_add_f32 v[50:51], v[50:51], v[6:7]
	v_cvt_pk_f32_fp8_e32 v[6:7], v100
	v_pk_add_f32 v[48:49], v[48:49], v[98:99]
	v_cvt_pk_f32_fp8_sdwa v[98:99], v101 src0_sel:WORD_1
	v_cvt_pk_f32_fp8_sdwa v[78:79], v100 src0_sel:WORD_1
	v_pk_mul_f32 v[52:53], v[76:77], v[52:53] op_sel_hi:[0,1]
	v_lshlrev_b32_e32 v100, 16, v4
	v_and_b32_e32 v101, 0xffff0000, v4
	v_pk_fma_f32 v[6:7], v[54:55], v[6:7], v[52:53] op_sel_hi:[0,1,1]
	v_pk_add_f32 v[52:53], v[6:7], v[100:101]
	v_pk_mul_f32 v[6:7], v[76:77], v[98:99] op_sel_hi:[0,1]
	v_lshlrev_b32_e32 v4, 16, v5
	v_and_b32_e32 v5, 0xffff0000, v5
	v_pk_fma_f32 v[6:7], v[54:55], v[78:79], v[6:7] op_sel_hi:[0,1,1]
	v_pk_add_f32 v[54:55], v[6:7], v[4:5]
	v_mov_b32_e32 v6, v57
	v_mov_b32_e32 v7, v59
	v_mov_b32_e32 v4, v56
	v_mov_b32_e32 v5, v58
	v_pk_mul_f32 v[6:7], v[6:7], v[6:7]
	v_mov_b32_e32 v78, v63
	v_mov_b32_e32 v79, v67
	v_pk_fma_f32 v[4:5], v[4:5], v[4:5], v[6:7]
	v_mov_b32_e32 v6, v62
	v_mov_b32_e32 v7, v66
	v_pk_mul_f32 v[78:79], v[78:79], v[78:79]
	v_mul_f32_e32 v76, v65, v65
	v_pk_fma_f32 v[6:7], v[6:7], v[6:7], v[78:79]
	v_mov_b32_e32 v78, v61
	v_mov_b32_e32 v79, v71
	v_pk_add_f32 v[4:5], v[4:5], v[6:7]
	v_mov_b32_e32 v6, v60
	v_mov_b32_e32 v7, v70
	v_pk_mul_f32 v[78:79], v[78:79], v[78:79]
	v_pk_add_f32 v[4:5], v[4:5], v[4:5] op_sel:[0,1] op_sel_hi:[1,0]
	v_pk_fma_f32 v[6:7], v[6:7], v[6:7], v[78:79]
	v_pk_fma_f32 v[78:79], v[64:65], v[64:65], v[76:77] op_sel_hi:[1,1,0]
	v_mul_f32_e32 v76, v73, v73
	v_pk_add_f32 v[6:7], v[6:7], v[6:7] op_sel:[0,1] op_sel_hi:[1,0]
	v_pk_fma_f32 v[98:99], v[72:73], v[72:73], v[76:77] op_sel_hi:[1,1,0]
	v_pk_mul_f32 v[100:101], v[68:69], v[68:69]
	v_pk_mul_f32 v[102:103], v[74:75], v[74:75]
	v_mov_b32_e32 v5, v100
	v_mov_b32_e32 v7, v101
	v_mov_b32_e32 v79, v102
	v_mov_b32_e32 v99, v103
	v_pk_add_f32 v[4:5], v[4:5], v[6:7]
	v_pk_add_f32 v[6:7], v[78:79], v[98:99]
	v_mov_b32_e32 v78, v45
	v_mov_b32_e32 v79, v47
	v_pk_add_f32 v[4:5], v[4:5], v[6:7]
	v_mov_b32_e32 v6, v44
	v_mov_b32_e32 v7, v46
	v_pk_mul_f32 v[78:79], v[78:79], v[78:79]
	v_mul_f32_e32 v76, v49, v49
	v_pk_fma_f32 v[6:7], v[6:7], v[6:7], v[78:79]
	v_pk_fma_f32 v[78:79], v[48:49], v[48:49], v[76:77] op_sel_hi:[1,1,0]
	v_mul_f32_e32 v76, v51, v51
	v_pk_add_f32 v[4:5], v[4:5], v[4:5] op_sel:[0,1] op_sel_hi:[1,0]
	v_pk_add_f32 v[6:7], v[6:7], v[6:7] op_sel:[0,1] op_sel_hi:[1,0]
	v_pk_fma_f32 v[98:99], v[50:51], v[50:51], v[76:77] op_sel_hi:[1,1,0]
	v_pk_mul_f32 v[100:101], v[52:53], v[52:53]
	v_pk_mul_f32 v[102:103], v[54:55], v[54:55]
	v_mov_b32_e32 v5, v100
	v_mov_b32_e32 v7, v101
	v_mov_b32_e32 v79, v102
	v_mov_b32_e32 v99, v103
	v_pk_add_f32 v[4:5], v[4:5], v[6:7]
	v_pk_add_f32 v[6:7], v[78:79], v[98:99]
	s_nop 0
	v_pk_add_f32 v[4:5], v[4:5], v[6:7]
	s_nop 0
	v_add_f32_e32 v4, v4, v5
	ds_bpermute_b32 v5, v3, v4
	s_waitcnt lgkmcnt(0)
; #define GAS __attribute__((address_space(1)))
; __device__ __forceinline__ unsigned pk2(float lo, float hi) { f32x2_m v = {lo, hi}; bf16x2_m b = __builtin_convertvector(v, bf16x2_m); return __builtin_bit_cast(unsigned, b); }
; template <int MODE, bool W8 = false>
; __device__ __forceinline__ void norm_rows(const Ctx& C, const void* src, bf16* xdst, const unsigned char* YS8, const int* srow, const float* gate, const float* gain, bf16* XN, float* outf, unsigned char* XN8 = nullptr) {
;     ...
;             for (int j = 0; j < 8; ++j) ss += (v[q][j].x * v[q][j].x + v[q][j].y * v[q][j].y) + (v[q][j].z * v[q][j].z + v[q][j].w * v[q][j].w);
;             const float rstd = 1.0f / sqrtf(wave_sum(ss) * (1.0f / DM) + RMS_EPS);
;             if (MODE == 1) { GAS v2u* xo = (GAS v2u*)(xdst + (size_t)m * DM) + C.lane;
; #pragma unroll
;                 for (int j = 0; j < 8; ++j) { v2u w; w.x = pk2(v[q][j].x, v[q][j].y); w.y = pk2(v[q][j].z, v[q][j].w); xo[64 * j] = w; } }
;             const GAS f32x4* gg = (const GAS f32x4*)gain + C.lane;
;             if (MODE <= 1) { GAS v2u* o = (GAS v2u*)(XN + (size_t)m * DM) + C.lane;
; #pragma unroll
;                 for (int j = 0; j < 8; ++j) { const f32x4 g = gg[64 * j]; const f32x4 y = v[q][j] * rstd * g; v2u w; w.x = pk2(y.x, y.y); w.y = pk2(y.z, y.w); o[64 * j] = w;
;                     if constexpr (W8) ((GAS unsigned*)(XN8 + (size_t)m * DM) + C.lane)[64 * j] = pk4_fp8m(y.x * SXN, y.y * SXN, y.z * SXN, y.w * SXN); } }
;             else { GAS f32x4* o = (GAS f32x4*)(outf + (size_t)m * DM) + C.lane;
; #pragma unroll
;                 for (int j = 0; j < 8; ++j) { const f32x4 g = gg[64 * j]; o[64 * j] = v[q][j] * rstd * g; } } }
	v_add_f32_e32 v4, v4, v5
	ds_bpermute_b32 v5, v27, v4
	s_waitcnt lgkmcnt(0)
	v_add_f32_e32 v4, v4, v5
	ds_bpermute_b32 v5, v77, v4
	s_waitcnt lgkmcnt(0)
	v_add_f32_e32 v4, v4, v5
	ds_bpermute_b32 v5, v80, v4
	s_waitcnt lgkmcnt(0)
	v_add_f32_e32 v4, v4, v5
	ds_bpermute_b32 v5, v81, v4
	s_waitcnt lgkmcnt(0)
	v_add_f32_e32 v4, v4, v5
	ds_bpermute_b32 v5, v82, v4
	s_waitcnt lgkmcnt(0)
	v_add_f32_e32 v4, v4, v5
	v_fmamk_f32 v4, v4, 0x3a000000, v212
	v_cmp_gt_f32_e32 vcc, s30, v4
	v_mul_f32_e32 v5, 0x4f800000, v4
	s_nop 0
	v_cndmask_b32_e32 v4, v4, v5, vcc
	v_sqrt_f32_e32 v5, v4
	s_nop 0
	v_add_u32_e32 v6, -1, v5
	v_fma_f32 v7, -v6, v5, v4
	v_cmp_ge_f32_e64 s[2:3], 0, v7
	v_add_u32_e32 v7, 1, v5
	s_nop 0
	v_cndmask_b32_e64 v6, v5, v6, s[2:3]
	v_fma_f32 v5, -v7, v5, v4
	v_cmp_lt_f32_e64 s[2:3], 0, v5
	s_nop 1
	v_cndmask_b32_e64 v5, v6, v7, s[2:3]
	v_mul_f32_e32 v6, 0x37800000, v5
	v_cndmask_b32_e32 v5, v5, v6, vcc
	v_cmp_class_f32_e32 vcc, v4, v211
	s_nop 1
	v_cndmask_b32_e32 v4, v5, v4, vcc
	v_div_scale_f32 v5, s[2:3], v4, v4, 1.0
	v_rcp_f32_e32 v6, v5
	s_nop 0
	v_fma_f32 v7, -v5, v6, 1.0
	v_fmac_f32_e32 v6, v7, v6
	v_div_scale_f32 v7, vcc, 1.0, v4, 1.0
	v_mul_f32_e32 v76, v7, v6
	v_fma_f32 v78, -v5, v76, v7
	v_fmac_f32_e32 v76, v78, v6
	v_fma_f32 v5, -v5, v76, v7
	v_div_fmas_f32 v5, v5, v6, v76
	v_div_fixup_f32 v76, v5, v4, 1.0
	v_pk_mul_f32 v[56:57], v[56:57], v[76:77] op_sel_hi:[1,0]
	v_pk_mul_f32 v[62:63], v[62:63], v[76:77] op_sel_hi:[1,0]
	v_lshl_add_u64 v[78:79], s[20:21], 0, v[0:1]
	v_pk_mul_f32 v[58:59], v[58:59], v[76:77] op_sel_hi:[1,0]
	v_pk_mul_f32 v[46:47], v[46:47], v[76:77] op_sel_hi:[1,0]
	v_pk_mul_f32 v[44:45], v[44:45], v[76:77] op_sel_hi:[1,0]
	v_pk_mul_f32 v[6:7], v[162:163], v[62:63]
	v_pk_mul_f32 v[4:5], v[160:161], v[56:57]
	global_store_dwordx4 v[78:79], v[4:7], off
	s_nop 1
	v_pk_mul_f32 v[56:57], v[66:67], v[76:77] op_sel_hi:[1,0]
	v_lshlrev_b32_e32 v62, 16, v24
	v_and_b32_e32 v63, 0xffff0000, v24
	v_lshlrev_b32_e32 v24, 16, v25
	v_and_b32_e32 v25, 0xffff0000, v25
	v_pk_mul_f32 v[4:5], v[164:165], v[58:59]
	v_pk_mul_f32 v[6:7], v[166:167], v[56:57]
	global_store_dwordx4 v[78:79], v[4:7], off offset:1024
	s_nop 1
	v_pk_mul_f32 v[56:57], v[70:71], v[76:77] op_sel_hi:[1,0]
	v_pk_mul_f32 v[58:59], v[60:61], v[76:77] op_sel_hi:[1,0]
	v_lshlrev_b32_e32 v60, 16, v30
	v_and_b32_e32 v61, 0xffff0000, v30
	v_lshlrev_b32_e32 v30, 16, v31
	v_and_b32_e32 v31, 0xffff0000, v31
	v_pk_mul_f32 v[4:5], v[168:169], v[58:59]
	v_pk_mul_f32 v[6:7], v[170:171], v[56:57]
	global_store_dwordx4 v[78:79], v[4:7], off offset:2048
	s_nop 1
	v_pk_mul_f32 v[56:57], v[72:73], v[76:77] op_sel_hi:[1,0]
	v_pk_mul_f32 v[58:59], v[64:65], v[76:77] op_sel_hi:[1,0]
	v_pk_mul_f32 v[6:7], v[174:175], v[56:57]
	v_pk_mul_f32 v[4:5], v[172:173], v[58:59]
	global_store_dwordx4 v[78:79], v[4:7], off offset:3072
	s_nop 1
	v_pk_mul_f32 v[56:57], v[74:75], v[76:77] op_sel_hi:[1,0]
	v_pk_mul_f32 v[58:59], v[68:69], v[76:77] op_sel_hi:[1,0]
	v_pk_mul_f32 v[6:7], v[178:179], v[56:57]
	v_add_co_u32_e32 v56, vcc, s27, v78
	v_pk_mul_f32 v[4:5], v[176:177], v[58:59]
	s_nop 0
	v_addc_co_u32_e32 v57, vcc, 0, v79, vcc
	global_store_dwordx4 v[56:57], v[4:7], off
	s_nop 1
	v_lshlrev_b32_e32 v58, 16, v32
	v_and_b32_e32 v59, 0xffff0000, v32
	v_lshlrev_b32_e32 v32, 16, v33
	v_and_b32_e32 v33, 0xffff0000, v33
	v_pk_mul_f32 v[4:5], v[180:181], v[44:45]
	v_pk_mul_f32 v[6:7], v[182:183], v[46:47]
	global_store_dwordx4 v[56:57], v[4:7], off offset:1024
	s_nop 1
	v_pk_mul_f32 v[44:45], v[50:51], v[76:77] op_sel_hi:[1,0]
	v_pk_mul_f32 v[46:47], v[48:49], v[76:77] op_sel_hi:[1,0]
	v_lshlrev_b32_e32 v48, 16, v42
	v_and_b32_e32 v49, 0xffff0000, v42
	v_lshlrev_b32_e32 v50, 16, v40
	v_and_b32_e32 v51, 0xffff0000, v40
	v_pk_mul_f32 v[4:5], v[184:185], v[46:47]
	v_pk_mul_f32 v[6:7], v[186:187], v[44:45]
	global_store_dwordx4 v[56:57], v[4:7], off offset:2048
	s_nop 1
	v_pk_mul_f32 v[44:45], v[54:55], v[76:77] op_sel_hi:[1,0]
	v_pk_mul_f32 v[46:47], v[52:53], v[76:77] op_sel_hi:[1,0]
	v_lshlrev_b32_e32 v52, 16, v38
	v_and_b32_e32 v53, 0xffff0000, v38
	v_lshlrev_b32_e32 v54, 16, v36
	v_and_b32_e32 v55, 0xffff0000, v36
	v_pk_mul_f32 v[4:5], v[188:189], v[46:47]
	v_pk_mul_f32 v[6:7], v[190:191], v[44:45]
	s_waitcnt vmcnt(7)
; template <int MODE, bool W8 = false>
; __device__ __forceinline__ void norm_rows(const Ctx& C, const void* src, bf16* xdst, const unsigned char* YS8, const int* srow, const float* gate, const float* gain, bf16* XN, float* outf, unsigned char* XN8 = nullptr) {
;     ...
;                 for (int j = 0; j < 8; ++j) { const unsigned a = ya[q][j], b = yb[q][j];
;                     const f32x2_m a01 = __builtin_amdgcn_cvt_pk_f32_fp8((int)a, false), a23 = __builtin_amdgcn_cvt_pk_f32_fp8((int)a, true), b01 = __builtin_amdgcn_cvt_pk_f32_fp8((int)b, false), b23 = __builtin_amdgcn_cvt_pk_f32_fp8((int)b, true);
;                     v[q][j].x += h0[q] * a01.x + h1[q] * b01.x; v[q][j].y += h0[q] * a01.y + h1[q] * b01.y; v[q][j].z += h0[q] * a23.x + h1[q] * b23.x; v[q][j].w += h0[q] * a23.y + h1[q] * b23.y; } }
;             float ss = 0.f;
; #pragma unroll
;             for (int j = 0; j < 8; ++j) ss += (v[q][j].x * v[q][j].x + v[q][j].y * v[q][j].y) + (v[q][j].z * v[q][j].z + v[q][j].w * v[q][j].w);
	v_cvt_pk_f32_fp8_e32 v[44:45], v95
	global_store_dwordx4 v[56:57], v[4:7], off offset:3072
	s_nop 1
	v_cvt_pk_f32_fp8_sdwa v[46:47], v95 src0_sel:WORD_1
	v_lshlrev_b32_e32 v56, 16, v34
	v_cvt_pk_f32_fp8_e32 v[4:5], v96
	v_cvt_pk_f32_fp8_sdwa v[6:7], v96 src0_sel:WORD_1
	v_pk_mul_f32 v[44:45], v[28:29], v[44:45] op_sel_hi:[0,1]
	v_and_b32_e32 v57, 0xffff0000, v34
	v_pk_fma_f32 v[4:5], v[26:27], v[4:5], v[44:45] op_sel_hi:[0,1,1]
	v_pk_add_f32 v[44:45], v[4:5], v[48:49]
	v_lshlrev_b32_e32 v4, 16, v43
	v_and_b32_e32 v5, 0xffff0000, v43
	v_pk_mul_f32 v[42:43], v[28:29], v[46:47] op_sel_hi:[0,1]
	v_pk_fma_f32 v[6:7], v[26:27], v[6:7], v[42:43] op_sel_hi:[0,1,1]
	v_cvt_pk_f32_fp8_e32 v[42:43], v93
	v_pk_add_f32 v[46:47], v[6:7], v[4:5]
	v_cvt_pk_f32_fp8_e32 v[4:5], v94
	v_cvt_pk_f32_fp8_sdwa v[48:49], v93 src0_sel:WORD_1
	v_cvt_pk_f32_fp8_sdwa v[6:7], v94 src0_sel:WORD_1
	v_pk_mul_f32 v[42:43], v[28:29], v[42:43] op_sel_hi:[0,1]
	v_pk_fma_f32 v[4:5], v[26:27], v[4:5], v[42:43] op_sel_hi:[0,1,1]
	v_pk_add_f32 v[42:43], v[4:5], v[50:51]
	v_lshlrev_b32_e32 v4, 16, v41
	v_and_b32_e32 v5, 0xffff0000, v41
	v_pk_mul_f32 v[40:41], v[28:29], v[48:49] op_sel_hi:[0,1]
	v_pk_fma_f32 v[6:7], v[26:27], v[6:7], v[40:41] op_sel_hi:[0,1,1]
	v_cvt_pk_f32_fp8_e32 v[40:41], v91
	v_pk_add_f32 v[48:49], v[6:7], v[4:5]
	v_cvt_pk_f32_fp8_e32 v[4:5], v92
	v_cvt_pk_f32_fp8_sdwa v[50:51], v91 src0_sel:WORD_1
	v_cvt_pk_f32_fp8_sdwa v[6:7], v92 src0_sel:WORD_1
	v_pk_mul_f32 v[40:41], v[28:29], v[40:41] op_sel_hi:[0,1]
	v_pk_fma_f32 v[4:5], v[26:27], v[4:5], v[40:41] op_sel_hi:[0,1,1]
	v_pk_add_f32 v[40:41], v[4:5], v[52:53]
	v_lshlrev_b32_e32 v4, 16, v39
	v_and_b32_e32 v5, 0xffff0000, v39
	v_pk_mul_f32 v[38:39], v[28:29], v[50:51] op_sel_hi:[0,1]
	v_pk_fma_f32 v[6:7], v[26:27], v[6:7], v[38:39] op_sel_hi:[0,1,1]
	v_cvt_pk_f32_fp8_e32 v[38:39], v89
	v_pk_add_f32 v[50:51], v[6:7], v[4:5]
	v_cvt_pk_f32_fp8_e32 v[4:5], v90
	v_cvt_pk_f32_fp8_sdwa v[52:53], v89 src0_sel:WORD_1
	v_cvt_pk_f32_fp8_sdwa v[6:7], v90 src0_sel:WORD_1
	v_pk_mul_f32 v[38:39], v[28:29], v[38:39] op_sel_hi:[0,1]
	v_pk_fma_f32 v[4:5], v[26:27], v[4:5], v[38:39] op_sel_hi:[0,1,1]
	v_pk_add_f32 v[38:39], v[4:5], v[54:55]
	v_lshlrev_b32_e32 v4, 16, v37
	v_and_b32_e32 v5, 0xffff0000, v37
	v_pk_mul_f32 v[36:37], v[28:29], v[52:53] op_sel_hi:[0,1]
	v_pk_fma_f32 v[6:7], v[26:27], v[6:7], v[36:37] op_sel_hi:[0,1,1]
	v_cvt_pk_f32_fp8_e32 v[36:37], v87
	v_pk_add_f32 v[52:53], v[6:7], v[4:5]
	v_cvt_pk_f32_fp8_e32 v[4:5], v88
	v_cvt_pk_f32_fp8_sdwa v[54:55], v87 src0_sel:WORD_1
	v_cvt_pk_f32_fp8_sdwa v[6:7], v88 src0_sel:WORD_1
	v_pk_mul_f32 v[36:37], v[28:29], v[36:37] op_sel_hi:[0,1]
	v_pk_fma_f32 v[4:5], v[26:27], v[4:5], v[36:37] op_sel_hi:[0,1,1]
	v_pk_add_f32 v[36:37], v[4:5], v[56:57]
	v_lshlrev_b32_e32 v4, 16, v35
	v_and_b32_e32 v5, 0xffff0000, v35
	v_pk_mul_f32 v[34:35], v[28:29], v[54:55] op_sel_hi:[0,1]
	v_pk_fma_f32 v[6:7], v[26:27], v[6:7], v[34:35] op_sel_hi:[0,1,1]
	v_cvt_pk_f32_fp8_e32 v[34:35], v85
	v_pk_add_f32 v[54:55], v[6:7], v[4:5]
	v_cvt_pk_f32_fp8_e32 v[4:5], v86
	v_cvt_pk_f32_fp8_sdwa v[56:57], v85 src0_sel:WORD_1
	v_cvt_pk_f32_fp8_sdwa v[6:7], v86 src0_sel:WORD_1
	v_pk_mul_f32 v[34:35], v[28:29], v[34:35] op_sel_hi:[0,1]
	v_pk_fma_f32 v[4:5], v[26:27], v[4:5], v[34:35] op_sel_hi:[0,1,1]
	v_pk_mul_f32 v[34:35], v[28:29], v[56:57] op_sel_hi:[0,1]
	v_pk_fma_f32 v[6:7], v[26:27], v[6:7], v[34:35] op_sel_hi:[0,1,1]
	v_cvt_pk_f32_fp8_e32 v[56:57], v83
	v_pk_add_f32 v[32:33], v[6:7], v[32:33]
	v_cvt_pk_f32_fp8_e32 v[6:7], v84
	v_pk_add_f32 v[4:5], v[4:5], v[58:59]
	v_cvt_pk_f32_fp8_sdwa v[58:59], v83 src0_sel:WORD_1
	v_cvt_pk_f32_fp8_sdwa v[34:35], v84 src0_sel:WORD_1
	v_pk_mul_f32 v[56:57], v[28:29], v[56:57] op_sel_hi:[0,1]
	v_pk_fma_f32 v[6:7], v[26:27], v[6:7], v[56:57] op_sel_hi:[0,1,1]
	v_pk_add_f32 v[6:7], v[6:7], v[60:61]
	v_pk_mul_f32 v[56:57], v[28:29], v[58:59] op_sel_hi:[0,1]
	v_cvt_pk_f32_fp8_e32 v[58:59], v17
	v_cvt_pk_f32_fp8_sdwa v[60:61], v17 src0_sel:WORD_1
	v_pk_fma_f32 v[34:35], v[26:27], v[34:35], v[56:57] op_sel_hi:[0,1,1]
	v_cvt_pk_f32_fp8_sdwa v[56:57], v29 src0_sel:WORD_1
	v_pk_add_f32 v[34:35], v[34:35], v[30:31]
	v_cvt_pk_f32_fp8_e32 v[30:31], v29
	v_pk_mul_f32 v[58:59], v[28:29], v[58:59] op_sel_hi:[0,1]
	v_pk_mul_f32 v[28:29], v[28:29], v[60:61] op_sel_hi:[0,1]
	v_pk_fma_f32 v[28:29], v[26:27], v[56:57], v[28:29] op_sel_hi:[0,1,1]
	v_mov_b32_e32 v56, v45
	v_mov_b32_e32 v57, v43
	v_pk_fma_f32 v[30:31], v[26:27], v[30:31], v[58:59] op_sel_hi:[0,1,1]
	v_pk_add_f32 v[24:25], v[28:29], v[24:25]
	v_mov_b32_e32 v28, v44
	v_mov_b32_e32 v29, v42
	v_pk_mul_f32 v[56:57], v[56:57], v[56:57]
	v_mov_b32_e32 v58, v47
	v_mov_b32_e32 v59, v49
	v_pk_fma_f32 v[28:29], v[28:29], v[28:29], v[56:57]
	v_mov_b32_e32 v56, v46
	v_mov_b32_e32 v57, v48
	v_pk_mul_f32 v[58:59], v[58:59], v[58:59]
	v_mul_f32_e32 v26, v39, v39
	v_pk_fma_f32 v[56:57], v[56:57], v[56:57], v[58:59]
	v_mov_b32_e32 v58, v41
	v_mov_b32_e32 v59, v51
	v_pk_add_f32 v[28:29], v[28:29], v[56:57]
	v_mov_b32_e32 v56, v40
	v_mov_b32_e32 v57, v50
	v_pk_mul_f32 v[58:59], v[58:59], v[58:59]
	v_pk_add_f32 v[30:31], v[30:31], v[62:63]
	v_pk_fma_f32 v[56:57], v[56:57], v[56:57], v[58:59]
	v_pk_fma_f32 v[58:59], v[38:39], v[38:39], v[26:27] op_sel_hi:[1,1,0]
	v_mul_f32_e32 v26, v53, v53
	v_pk_add_f32 v[28:29], v[28:29], v[28:29] op_sel:[0,1] op_sel_hi:[1,0]
	v_pk_add_f32 v[56:57], v[56:57], v[56:57] op_sel:[0,1] op_sel_hi:[1,0]
	v_pk_fma_f32 v[60:61], v[52:53], v[52:53], v[26:27] op_sel_hi:[1,1,0]
	v_pk_mul_f32 v[62:63], v[36:37], v[36:37]
	v_pk_mul_f32 v[64:65], v[54:55], v[54:55]
	v_mov_b32_e32 v29, v62
	v_mov_b32_e32 v57, v63
	v_mov_b32_e32 v59, v64
	v_mov_b32_e32 v61, v65
	v_pk_add_f32 v[28:29], v[28:29], v[56:57]
	v_pk_add_f32 v[56:57], v[58:59], v[60:61]
	v_mov_b32_e32 v58, v5
	v_mov_b32_e32 v59, v33
	v_pk_add_f32 v[28:29], v[28:29], v[56:57]
	v_mov_b32_e32 v56, v4
	v_mov_b32_e32 v57, v32
	v_pk_mul_f32 v[58:59], v[58:59], v[58:59]
	v_mul_f32_e32 v26, v7, v7
	v_pk_fma_f32 v[56:57], v[56:57], v[56:57], v[58:59]
	v_pk_fma_f32 v[58:59], v[6:7], v[6:7], v[26:27] op_sel_hi:[1,1,0]
	v_mul_f32_e32 v26, v35, v35
	v_pk_add_f32 v[28:29], v[28:29], v[28:29] op_sel:[0,1] op_sel_hi:[1,0]
	v_pk_add_f32 v[56:57], v[56:57], v[56:57] op_sel:[0,1] op_sel_hi:[1,0]
	v_pk_fma_f32 v[60:61], v[34:35], v[34:35], v[26:27] op_sel_hi:[1,1,0]
	v_pk_mul_f32 v[62:63], v[30:31], v[30:31]
	v_pk_mul_f32 v[64:65], v[24:25], v[24:25]
	v_mov_b32_e32 v29, v62
	v_mov_b32_e32 v57, v63
	v_mov_b32_e32 v59, v64
	v_mov_b32_e32 v61, v65
	v_pk_add_f32 v[28:29], v[28:29], v[56:57]
	v_pk_add_f32 v[56:57], v[58:59], v[60:61]
	s_nop 0
	v_pk_add_f32 v[28:29], v[28:29], v[56:57]
	s_nop 0
	v_add_f32_e32 v17, v28, v29
	ds_bpermute_b32 v26, v3, v17
	s_waitcnt lgkmcnt(0)
; #define GAS __attribute__((address_space(1)))
; __device__ __forceinline__ unsigned pk2(float lo, float hi) { f32x2_m v = {lo, hi}; bf16x2_m b = __builtin_convertvector(v, bf16x2_m); return __builtin_bit_cast(unsigned, b); }
; template <int MODE, bool W8 = false>
; __device__ __forceinline__ void norm_rows(const Ctx& C, const void* src, bf16* xdst, const unsigned char* YS8, const int* srow, const float* gate, const float* gain, bf16* XN, float* outf, unsigned char* XN8 = nullptr) {
;     ...
;             for (int j = 0; j < 8; ++j) ss += (v[q][j].x * v[q][j].x + v[q][j].y * v[q][j].y) + (v[q][j].z * v[q][j].z + v[q][j].w * v[q][j].w);
;             const float rstd = 1.0f / sqrtf(wave_sum(ss) * (1.0f / DM) + RMS_EPS);
;             if (MODE == 1) { GAS v2u* xo = (GAS v2u*)(xdst + (size_t)m * DM) + C.lane;
; #pragma unroll
;                 for (int j = 0; j < 8; ++j) { v2u w; w.x = pk2(v[q][j].x, v[q][j].y); w.y = pk2(v[q][j].z, v[q][j].w); xo[64 * j] = w; } }
;             const GAS f32x4* gg = (const GAS f32x4*)gain + C.lane;
;             if (MODE <= 1) { GAS v2u* o = (GAS v2u*)(XN + (size_t)m * DM) + C.lane;
; #pragma unroll
;                 for (int j = 0; j < 8; ++j) { const f32x4 g = gg[64 * j]; const f32x4 y = v[q][j] * rstd * g; v2u w; w.x = pk2(y.x, y.y); w.y = pk2(y.z, y.w); o[64 * j] = w;
;                     if constexpr (W8) ((GAS unsigned*)(XN8 + (size_t)m * DM) + C.lane)[64 * j] = pk4_fp8m(y.x * SXN, y.y * SXN, y.z * SXN, y.w * SXN); } }
;             else { GAS f32x4* o = (GAS f32x4*)(outf + (size_t)m * DM) + C.lane;
; #pragma unroll
;                 for (int j = 0; j < 8; ++j) { const f32x4 g = gg[64 * j]; o[64 * j] = v[q][j] * rstd * g; } } }
	v_add_f32_e32 v17, v17, v26
	ds_bpermute_b32 v26, v27, v17
	s_waitcnt lgkmcnt(0)
	v_add_f32_e32 v17, v17, v26
	ds_bpermute_b32 v26, v77, v17
	s_waitcnt lgkmcnt(0)
	v_add_f32_e32 v17, v17, v26
	ds_bpermute_b32 v26, v80, v17
	s_waitcnt lgkmcnt(0)
	v_add_f32_e32 v17, v17, v26
	ds_bpermute_b32 v26, v81, v17
	s_waitcnt lgkmcnt(0)
	v_add_f32_e32 v17, v17, v26
	ds_bpermute_b32 v26, v82, v17
	s_waitcnt lgkmcnt(0)
	v_add_f32_e32 v17, v17, v26
	v_fmamk_f32 v17, v17, 0x3a000000, v212
	v_cmp_gt_f32_e32 vcc, s30, v17
	v_mul_f32_e32 v26, 0x4f800000, v17
	s_nop 0
	v_cndmask_b32_e32 v17, v17, v26, vcc
	v_sqrt_f32_e32 v26, v17
	s_nop 0
	v_add_u32_e32 v28, -1, v26
	v_fma_f32 v29, -v28, v26, v17
	v_cmp_ge_f32_e64 s[2:3], 0, v29
	v_add_u32_e32 v29, 1, v26
	s_nop 0
	v_cndmask_b32_e64 v28, v26, v28, s[2:3]
	v_fma_f32 v26, -v29, v26, v17
	v_cmp_lt_f32_e64 s[2:3], 0, v26
	s_nop 1
	v_cndmask_b32_e64 v26, v28, v29, s[2:3]
	v_mul_f32_e32 v28, 0x37800000, v26
	v_cndmask_b32_e32 v26, v26, v28, vcc
	v_cmp_class_f32_e32 vcc, v17, v211
	s_nop 1
	v_cndmask_b32_e32 v17, v26, v17, vcc
	v_div_scale_f32 v26, s[2:3], v17, v17, 1.0
	v_rcp_f32_e32 v28, v26
	s_nop 0
	v_fma_f32 v29, -v26, v28, 1.0
	v_fmac_f32_e32 v28, v29, v28
	v_div_scale_f32 v29, vcc, 1.0, v17, 1.0
	v_mul_f32_e32 v56, v29, v28
	v_fma_f32 v57, -v26, v56, v29
	v_fmac_f32_e32 v56, v57, v28
	v_fma_f32 v26, -v26, v56, v29
	v_div_fmas_f32 v26, v26, v28, v56
	v_div_fixup_f32 v26, v26, v17, 1.0
	v_pk_mul_f32 v[46:47], v[46:47], v[26:27] op_sel_hi:[1,0]
	v_pk_mul_f32 v[44:45], v[44:45], v[26:27] op_sel_hi:[1,0]
	v_lshl_add_u64 v[28:29], s[12:13], 0, v[0:1]
	v_pk_mul_f32 v[48:49], v[48:49], v[26:27] op_sel_hi:[1,0]
	v_pk_mul_f32 v[42:43], v[42:43], v[26:27] op_sel_hi:[1,0]
	v_pk_mul_f32 v[40:41], v[40:41], v[26:27] op_sel_hi:[1,0]
	v_pk_mul_f32 v[38:39], v[38:39], v[26:27] op_sel_hi:[1,0]
	v_pk_mul_f32 v[36:37], v[36:37], v[26:27] op_sel_hi:[1,0]
	v_pk_mul_f32 v[32:33], v[32:33], v[26:27] op_sel_hi:[1,0]
	v_pk_mul_f32 v[4:5], v[4:5], v[26:27] op_sel_hi:[1,0]
	s_add_u32 s12, s12, 0x2000000
	s_addc_u32 s13, s13, 0
	s_add_u32 s16, s16, 0x1000000
	s_addc_u32 s17, s17, 0
	s_add_u32 s18, s18, 0x1000000
	s_addc_u32 s19, s19, 0
	s_add_u32 s20, s20, 0x2000000
	v_pk_mul_f32 v[24:25], v[24:25], v[26:27] op_sel_hi:[1,0]
	v_pk_mul_f32 v[30:31], v[30:31], v[26:27] op_sel_hi:[1,0]
	s_addc_u32 s21, s21, 0
	s_cmpk_lt_i32 s26, 0x3000
	v_pk_mul_f32 v[44:45], v[160:161], v[44:45]
	v_pk_mul_f32 v[46:47], v[162:163], v[46:47]
	global_store_dwordx4 v[28:29], v[44:47], off
	s_nop 1
	v_pk_mul_f32 v[42:43], v[164:165], v[42:43]
	v_pk_mul_f32 v[44:45], v[166:167], v[48:49]
	global_store_dwordx4 v[28:29], v[42:45], off offset:1024
	s_nop 1
	v_pk_mul_f32 v[46:47], v[50:51], v[26:27] op_sel_hi:[1,0]
	v_pk_mul_f32 v[40:41], v[168:169], v[40:41]
	v_pk_mul_f32 v[42:43], v[170:171], v[46:47]
	global_store_dwordx4 v[28:29], v[40:43], off offset:2048
	s_nop 1
	v_pk_mul_f32 v[44:45], v[52:53], v[26:27] op_sel_hi:[1,0]
	v_pk_mul_f32 v[38:39], v[172:173], v[38:39]
	v_pk_mul_f32 v[40:41], v[174:175], v[44:45]
	global_store_dwordx4 v[28:29], v[38:41], off offset:3072
	s_nop 1
	v_pk_mul_f32 v[42:43], v[54:55], v[26:27] op_sel_hi:[1,0]
	v_add_co_u32_e32 v28, vcc, s27, v28
	v_pk_mul_f32 v[36:37], v[176:177], v[36:37]
	v_pk_mul_f32 v[38:39], v[178:179], v[42:43]
	v_addc_co_u32_e32 v29, vcc, 0, v29, vcc
	global_store_dwordx4 v[28:29], v[36:39], off
	s_nop 1
	v_pk_mul_f32 v[36:37], v[180:181], v[4:5]
	v_pk_mul_f32 v[38:39], v[182:183], v[32:33]
	global_store_dwordx4 v[28:29], v[36:39], off offset:1024
	s_nop 1
	v_pk_mul_f32 v[32:33], v[34:35], v[26:27] op_sel_hi:[1,0]
	v_pk_mul_f32 v[4:5], v[6:7], v[26:27] op_sel_hi:[1,0]
	v_pk_mul_f32 v[6:7], v[186:187], v[32:33]
	v_pk_mul_f32 v[4:5], v[184:185], v[4:5]
	global_store_dwordx4 v[28:29], v[4:7], off offset:2048
	s_nop 1
	v_pk_mul_f32 v[4:5], v[188:189], v[30:31]
	v_pk_mul_f32 v[6:7], v[190:191], v[24:25]
	global_store_dwordx4 v[28:29], v[4:7], off offset:3072
	s_nop 1
	s_cbranch_scc1 .LBB0_1321

; #define GAS __attribute__((address_space(1)))
; __device__ __forceinline__ float bflo(unsigned w) { return __uint_as_float(w << 16); }
; __device__ __forceinline__ float bfhi(unsigned w) { return __uint_as_float(w & 0xffff0000u); }
; template <int MODE, bool W8 = false>
; __device__ __forceinline__ void norm_rows(const Ctx& C, const void* src, bf16* xdst, const unsigned char* YS8, const int* srow, const float* gate, const float* gain, bf16* XN, float* outf, unsigned char* XN8 = nullptr) {
;     ...
;     for (int m0 = C.gw; m0 < T; m0 += NR * C.NGW) {
;         f32x4 v[NR][8]; unsigned ya[NR][8], yb[NR][8]; float h0[NR], h1[NR];
; #pragma unroll
;         for (int q = 0; q < NR; ++q) { const int m = m0 + q * C.NGW;
;             if (MODE == 0) { const GAS f32x4* xr = (const GAS f32x4*)((const float*)src + (size_t)m * DM) + C.lane;
; #pragma unroll
;                 for (int j = 0; j < 8; ++j) v[q][j] = xr[64 * j]; }
;             else { const GAS v2u* xr = (const GAS v2u*)((const bf16*)src + (size_t)m * DM) + C.lane;
; #pragma unroll
;                 for (int j = 0; j < 8; ++j) { const v2u t_ = xr[64 * j]; v[q][j] = (f32x4){bflo(t_.x), bfhi(t_.x), bflo(t_.y), bfhi(t_.y)}; } }
;             if (MODE >= 1) {
;                 h0[q] = gate[2 * m] * (1.0f / SY); h1[q] = gate[2 * m + 1] * (1.0f / SY);
;                 const GAS unsigned* y0 = (const GAS unsigned*)(YS8 + (size_t)srow[2 * m] * DM) + C.lane; const GAS unsigned* y1 = (const GAS unsigned*)(YS8 + (size_t)srow[2 * m + 1] * DM) + C.lane;
; #pragma unroll
;                 for (int j = 0; j < 8; ++j) { ya[q][j] = y0[64 * j]; yb[q][j] = y1[64 * j]; } } }
; #pragma unroll
;         for (int q = 0; q < NR; ++q) { const int m = m0 + q * C.NGW;
;             if (MODE >= 1) {
; #pragma unroll
;                 for (int j = 0; j < 8; ++j) { const unsigned a = ya[q][j], b = yb[q][j];
;                     const f32x2_m a01 = __builtin_amdgcn_cvt_pk_f32_fp8((int)a, false), a23 = __builtin_amdgcn_cvt_pk_f32_fp8((int)a, true), b01 = __builtin_amdgcn_cvt_pk_f32_fp8((int)b, false), b23 = __builtin_amdgcn_cvt_pk_f32_fp8((int)b, true);
;                     v[q][j].x += h0[q] * a01.x + h1[q] * b01.x; v[q][j].y += h0[q] * a01.y + h1[q] * b01.y; v[q][j].z += h0[q] * a23.x + h1[q] * b23.x; v[q][j].w += h0[q] * a23.y + h1[q] * b23.y; } }
.LBB0_1326:
	s_ashr_i32 s1, s0, 31
	s_lshl_b64 s[2:3], s[0:1], 2
	s_add_u32 s2, s22, s2
	s_addc_u32 s3, s23, s3
	global_load_dwordx2 v[194:195], v2, s[2:3]
	s_ashr_i32 s1, s0, 31
	v_lshl_add_u64 v[52:53], s[4:5], 0, v[20:21]
	s_lshl_b64 s[2:3], s[0:1], 2
	v_add_co_u32_e32 v50, vcc, 0x4b800000, v52
	s_add_u32 s6, s24, s2
	s_nop 0
	v_addc_co_u32_e32 v51, vcc, 0, v53, vcc
	s_addc_u32 s7, s25, s3
	global_load_dwordx2 v[64:65], v[50:51], off
	global_load_dwordx2 v[62:63], v[50:51], off offset:512
	global_load_dwordx2 v[60:61], v[50:51], off offset:1024
	global_load_dwordx2 v[58:59], v[50:51], off offset:1536
	global_load_dwordx2 v[48:49], v[50:51], off offset:2048
	global_load_dwordx2 v[46:47], v[50:51], off offset:2560
	global_load_dwordx2 v[42:43], v[50:51], off offset:3072
	global_load_dwordx2 v[44:45], v[50:51], off offset:3584
	global_load_dwordx2 v[22:23], v2, s[6:7]
	s_add_i32 s6, s0, 1
	s_ashr_i32 s7, s6, 31
	s_add_u32 s2, s22, s2
	s_addc_u32 s3, s23, s3
	v_lshl_add_u64 v[28:29], s[4:5], 0, v[16:17]
	v_add_co_u32_e32 v26, vcc, s13, v28
	v_lshl_add_u64 v[16:17], v[16:17], 0, s[20:21]
	s_nop 0
	v_addc_co_u32_e32 v27, vcc, 0, v29, vcc
	v_lshl_add_u64 v[20:21], v[20:21], 0, s[20:21]
	s_waitcnt vmcnt(8)
	v_lshlrev_b32_e32 v74, 16, v64
	v_and_b32_e32 v75, 0xffff0000, v64
	v_lshlrev_b32_e32 v64, 16, v65
	v_and_b32_e32 v65, 0xffff0000, v65
	s_waitcnt vmcnt(0)
	v_mul_f32_e32 v78, 0x3d800000, v22
	v_mov_b32_e32 v22, v194
	s_lshl_b64 s[2:3], s[6:7], 2
	s_add_u32 s2, s22, s2
	s_addc_u32 s3, s23, s3
	v_mov_b32_e32 v24, v195
	s_add_i32 s2, s0, 0x1000
	s_ashr_i32 s3, s2, 31
	v_mul_f32_e32 v80, 0x3d800000, v23
	s_lshl_b64 s[2:3], s[2:3], 2
	s_add_u32 s6, s24, s2
	s_addc_u32 s7, s25, s3
	s_waitcnt vmcnt(1)
	v_ashrrev_i32_e32 v23, 31, v22
	v_lshlrev_b64 v[22:23], 11, v[22:23]
	v_lshl_add_u64 v[22:23], v[0:1], 0, v[22:23]
	s_waitcnt vmcnt(0)
	v_ashrrev_i32_e32 v25, 31, v24
	v_lshlrev_b64 v[24:25], 11, v[24:25]
	v_lshl_add_u64 v[24:25], v[0:1], 0, v[24:25]
	global_load_dword v70, v[22:23], off
	global_load_dword v72, v[24:25], off
	global_load_dword v76, v[22:23], off offset:256
	global_load_dword v77, v[24:25], off offset:256
	global_load_dword v79, v[22:23], off offset:512
	global_load_dword v100, v[24:25], off offset:512
	global_load_dword v101, v[22:23], off offset:768
	global_load_dword v102, v[24:25], off offset:768
	global_load_dword v103, v[22:23], off offset:1024
	global_load_dword v108, v[24:25], off offset:1024
	global_load_dword v109, v[22:23], off offset:1280
	global_load_dword v110, v[24:25], off offset:1280
	global_load_dword v111, v[22:23], off offset:1536
	global_load_dword v112, v[24:25], off offset:1536
	global_load_dword v113, v[22:23], off offset:1792
	global_load_dword v114, v[24:25], off offset:1792
	global_load_dwordx2 v[40:41], v[26:27], off
	global_load_dwordx2 v[38:39], v[26:27], off offset:512
	global_load_dwordx2 v[36:37], v[26:27], off offset:1024
	global_load_dwordx2 v[34:35], v[26:27], off offset:1536
	global_load_dwordx2 v[32:33], v[26:27], off offset:2048
	global_load_dwordx2 v[30:31], v[26:27], off offset:2560
	global_load_dwordx2 v[22:23], v[26:27], off offset:3072
	global_load_dwordx2 v[24:25], v[26:27], off offset:3584
	global_load_dwordx2 v[54:55], v2, s[6:7]
	s_add_i32 s6, s0, 0x1001
	s_ashr_i32 s7, s6, 31
	s_add_u32 s2, s22, s2
	s_addc_u32 s3, s23, s3
	global_load_dword v66, v2, s[2:3]
	s_lshl_b64 s[2:3], s[6:7], 2
	s_add_u32 s2, s22, s2
	s_addc_u32 s3, s23, s3
	global_load_dword v68, v2, s[2:3]
	s_addk_i32 s8, 0x1000
	s_addk_i32 s0, 0x2000
	s_cmpk_gt_i32 s8, 0x2fff
	s_waitcnt vmcnt(2)
	v_mul_f32_e32 v56, 0x3d800000, v55
	v_mul_f32_e32 v54, 0x3d800000, v54
	s_waitcnt vmcnt(1)
	v_ashrrev_i32_e32 v67, 31, v66
	v_lshlrev_b64 v[66:67], 11, v[66:67]
	v_lshl_add_u64 v[66:67], v[0:1], 0, v[66:67]
	s_waitcnt vmcnt(0)
	v_ashrrev_i32_e32 v69, 31, v68
	v_lshlrev_b64 v[68:69], 11, v[68:69]
	v_lshl_add_u64 v[68:69], v[0:1], 0, v[68:69]
	global_load_dword v99, v[66:67], off
	global_load_dword v98, v[68:69], off
	global_load_dword v97, v[66:67], off offset:256
	global_load_dword v96, v[68:69], off offset:256
	global_load_dword v95, v[66:67], off offset:512
	global_load_dword v94, v[68:69], off offset:512
	global_load_dword v93, v[66:67], off offset:768
	global_load_dword v92, v[68:69], off offset:768
	global_load_dword v91, v[66:67], off offset:1024
	global_load_dword v90, v[68:69], off offset:1024
	global_load_dword v89, v[66:67], off offset:1280
	global_load_dword v88, v[68:69], off offset:1280
	global_load_dword v87, v[66:67], off offset:1536
	global_load_dword v86, v[68:69], off offset:1536
	global_load_dword v85, v[66:67], off offset:1792
	global_load_dword v55, v[68:69], off offset:1792
	v_cvt_pk_f32_fp8_e32 v[66:67], v70
	v_cvt_pk_f32_fp8_sdwa v[68:69], v70 src0_sel:WORD_1
	v_cvt_pk_f32_fp8_e32 v[70:71], v72
	v_cvt_pk_f32_fp8_sdwa v[72:73], v72 src0_sel:WORD_1
	v_pk_mul_f32 v[70:71], v[80:81], v[70:71] op_sel_hi:[0,1]
	v_pk_fma_f32 v[66:67], v[78:79], v[66:67], v[70:71] op_sel_hi:[0,1,1]
	v_pk_add_f32 v[104:105], v[66:67], v[74:75]
	v_pk_mul_f32 v[66:67], v[80:81], v[72:73] op_sel_hi:[0,1]
	v_pk_fma_f32 v[66:67], v[78:79], v[68:69], v[66:67] op_sel_hi:[0,1,1]
	v_cvt_pk_f32_fp8_e32 v[68:69], v77
	v_pk_add_f32 v[106:107], v[66:67], v[64:65]
	v_cvt_pk_f32_fp8_e32 v[64:65], v76
	v_cvt_pk_f32_fp8_sdwa v[70:71], v77 src0_sel:WORD_1
	v_cvt_pk_f32_fp8_sdwa v[66:67], v76 src0_sel:WORD_1
	v_pk_mul_f32 v[68:69], v[80:81], v[68:69] op_sel_hi:[0,1]
	v_lshlrev_b32_e32 v72, 16, v62
	v_and_b32_e32 v73, 0xffff0000, v62
	v_pk_fma_f32 v[64:65], v[78:79], v[64:65], v[68:69] op_sel_hi:[0,1,1]
	v_pk_add_f32 v[74:75], v[64:65], v[72:73]
; template <int MODE, bool W8 = false>
; __device__ __forceinline__ void norm_rows(const Ctx& C, const void* src, bf16* xdst, const unsigned char* YS8, const int* srow, const float* gate, const float* gain, bf16* XN, float* outf, unsigned char* XN8 = nullptr) {
;     ...
;                 for (int j = 0; j < 8; ++j) { const unsigned a = ya[q][j], b = yb[q][j];
;                     const f32x2_m a01 = __builtin_amdgcn_cvt_pk_f32_fp8((int)a, false), a23 = __builtin_amdgcn_cvt_pk_f32_fp8((int)a, true), b01 = __builtin_amdgcn_cvt_pk_f32_fp8((int)b, false), b23 = __builtin_amdgcn_cvt_pk_f32_fp8((int)b, true);
;                     v[q][j].x += h0[q] * a01.x + h1[q] * b01.x; v[q][j].y += h0[q] * a01.y + h1[q] * b01.y; v[q][j].z += h0[q] * a23.x + h1[q] * b23.x; v[q][j].w += h0[q] * a23.y + h1[q] * b23.y; } }
;             float ss = 0.f;
; #pragma unroll
;             for (int j = 0; j < 8; ++j) ss += (v[q][j].x * v[q][j].x + v[q][j].y * v[q][j].y) + (v[q][j].z * v[q][j].z + v[q][j].w * v[q][j].w);
	v_pk_mul_f32 v[64:65], v[80:81], v[70:71] op_sel_hi:[0,1]
	v_lshlrev_b32_e32 v62, 16, v63
	v_and_b32_e32 v63, 0xffff0000, v63
	v_pk_fma_f32 v[64:65], v[78:79], v[66:67], v[64:65] op_sel_hi:[0,1,1]
	v_cvt_pk_f32_fp8_e32 v[66:67], v100
	v_pk_add_f32 v[76:77], v[64:65], v[62:63]
	v_cvt_pk_f32_fp8_e32 v[62:63], v79
	v_cvt_pk_f32_fp8_sdwa v[68:69], v100 src0_sel:WORD_1
	v_cvt_pk_f32_fp8_sdwa v[64:65], v79 src0_sel:WORD_1
	v_pk_mul_f32 v[66:67], v[80:81], v[66:67] op_sel_hi:[0,1]
	v_lshlrev_b32_e32 v70, 16, v60
	v_and_b32_e32 v71, 0xffff0000, v60
	v_pk_fma_f32 v[62:63], v[78:79], v[62:63], v[66:67] op_sel_hi:[0,1,1]
	v_pk_add_f32 v[70:71], v[62:63], v[70:71]
	v_pk_mul_f32 v[62:63], v[80:81], v[68:69] op_sel_hi:[0,1]
	v_lshlrev_b32_e32 v60, 16, v61
	v_and_b32_e32 v61, 0xffff0000, v61
	v_pk_fma_f32 v[62:63], v[78:79], v[64:65], v[62:63] op_sel_hi:[0,1,1]
	v_cvt_pk_f32_fp8_e32 v[64:65], v102
	v_pk_add_f32 v[72:73], v[62:63], v[60:61]
	v_cvt_pk_f32_fp8_e32 v[60:61], v101
	v_cvt_pk_f32_fp8_sdwa v[68:69], v102 src0_sel:WORD_1
	v_cvt_pk_f32_fp8_sdwa v[62:63], v101 src0_sel:WORD_1
	v_pk_mul_f32 v[64:65], v[80:81], v[64:65] op_sel_hi:[0,1]
	v_lshlrev_b32_e32 v66, 16, v58
	v_and_b32_e32 v67, 0xffff0000, v58
	v_pk_fma_f32 v[60:61], v[78:79], v[60:61], v[64:65] op_sel_hi:[0,1,1]
	v_pk_add_f32 v[66:67], v[60:61], v[66:67]
	v_pk_mul_f32 v[60:61], v[80:81], v[68:69] op_sel_hi:[0,1]
	v_lshlrev_b32_e32 v58, 16, v59
	v_and_b32_e32 v59, 0xffff0000, v59
	v_pk_fma_f32 v[60:61], v[78:79], v[62:63], v[60:61] op_sel_hi:[0,1,1]
	v_cvt_pk_f32_fp8_e32 v[62:63], v108
	v_pk_add_f32 v[68:69], v[60:61], v[58:59]
	v_cvt_pk_f32_fp8_e32 v[58:59], v103
	v_cvt_pk_f32_fp8_sdwa v[64:65], v108 src0_sel:WORD_1
	v_cvt_pk_f32_fp8_sdwa v[60:61], v103 src0_sel:WORD_1
	v_pk_mul_f32 v[62:63], v[80:81], v[62:63] op_sel_hi:[0,1]
	v_lshlrev_b32_e32 v100, 16, v48
	v_and_b32_e32 v101, 0xffff0000, v48
	v_pk_fma_f32 v[58:59], v[78:79], v[58:59], v[62:63] op_sel_hi:[0,1,1]
	v_pk_add_f32 v[62:63], v[58:59], v[100:101]
	v_pk_mul_f32 v[58:59], v[80:81], v[64:65] op_sel_hi:[0,1]
	v_lshlrev_b32_e32 v48, 16, v49
	v_and_b32_e32 v49, 0xffff0000, v49
	v_pk_fma_f32 v[58:59], v[78:79], v[60:61], v[58:59] op_sel_hi:[0,1,1]
	v_pk_add_f32 v[64:65], v[58:59], v[48:49]
	v_cvt_pk_f32_fp8_e32 v[58:59], v110
	v_cvt_pk_f32_fp8_e32 v[48:49], v109
	v_cvt_pk_f32_fp8_sdwa v[100:101], v110 src0_sel:WORD_1
	v_cvt_pk_f32_fp8_sdwa v[60:61], v109 src0_sel:WORD_1
	v_pk_mul_f32 v[58:59], v[80:81], v[58:59] op_sel_hi:[0,1]
	v_lshlrev_b32_e32 v102, 16, v46
	v_and_b32_e32 v103, 0xffff0000, v46
	v_pk_fma_f32 v[48:49], v[78:79], v[48:49], v[58:59] op_sel_hi:[0,1,1]
	v_pk_add_f32 v[58:59], v[48:49], v[102:103]
	v_pk_mul_f32 v[48:49], v[80:81], v[100:101] op_sel_hi:[0,1]
	v_lshlrev_b32_e32 v46, 16, v47
	v_and_b32_e32 v47, 0xffff0000, v47
	v_pk_fma_f32 v[48:49], v[78:79], v[60:61], v[48:49] op_sel_hi:[0,1,1]
	v_cvt_pk_f32_fp8_e32 v[100:101], v112
	v_pk_add_f32 v[60:61], v[48:49], v[46:47]
	v_cvt_pk_f32_fp8_e32 v[46:47], v111
	v_cvt_pk_f32_fp8_sdwa v[102:103], v112 src0_sel:WORD_1
	v_cvt_pk_f32_fp8_sdwa v[48:49], v111 src0_sel:WORD_1
	v_pk_mul_f32 v[100:101], v[80:81], v[100:101] op_sel_hi:[0,1]
	v_pk_fma_f32 v[46:47], v[78:79], v[46:47], v[100:101] op_sel_hi:[0,1,1]
	v_pk_mul_f32 v[100:101], v[80:81], v[102:103] op_sel_hi:[0,1]
	v_lshlrev_b32_e32 v108, 16, v42
	v_and_b32_e32 v109, 0xffff0000, v42
	v_lshlrev_b32_e32 v42, 16, v43
	v_and_b32_e32 v43, 0xffff0000, v43
	v_pk_fma_f32 v[48:49], v[78:79], v[48:49], v[100:101] op_sel_hi:[0,1,1]
	v_cvt_pk_f32_fp8_e32 v[102:103], v114
	v_pk_add_f32 v[46:47], v[46:47], v[108:109]
	v_pk_add_f32 v[48:49], v[48:49], v[42:43]
	v_cvt_pk_f32_fp8_e32 v[42:43], v113
	v_cvt_pk_f32_fp8_sdwa v[108:109], v114 src0_sel:WORD_1
	v_cvt_pk_f32_fp8_sdwa v[100:101], v113 src0_sel:WORD_1
	v_pk_mul_f32 v[102:103], v[80:81], v[102:103] op_sel_hi:[0,1]
	v_pk_fma_f32 v[42:43], v[78:79], v[42:43], v[102:103] op_sel_hi:[0,1,1]
	v_pk_mul_f32 v[102:103], v[80:81], v[108:109] op_sel_hi:[0,1]
	v_lshlrev_b32_e32 v110, 16, v44
	v_and_b32_e32 v111, 0xffff0000, v44
	v_lshlrev_b32_e32 v44, 16, v45
	v_and_b32_e32 v45, 0xffff0000, v45
	v_pk_fma_f32 v[78:79], v[78:79], v[100:101], v[102:103] op_sel_hi:[0,1,1]
	v_mov_b32_e32 v100, v105
	v_mov_b32_e32 v101, v75
	v_pk_add_f32 v[44:45], v[78:79], v[44:45]
	v_mov_b32_e32 v78, v104
	v_mov_b32_e32 v79, v74
	v_pk_mul_f32 v[100:101], v[100:101], v[100:101]
	v_mov_b32_e32 v102, v107
	v_mov_b32_e32 v103, v77
	v_pk_fma_f32 v[78:79], v[78:79], v[78:79], v[100:101]
	v_mov_b32_e32 v100, v106
	v_mov_b32_e32 v101, v76
	v_pk_mul_f32 v[102:103], v[102:103], v[102:103]
	v_mul_f32_e32 v80, v67, v67
	v_pk_fma_f32 v[100:101], v[100:101], v[100:101], v[102:103]
	v_mov_b32_e32 v102, v71
	v_mov_b32_e32 v103, v73
	v_pk_add_f32 v[78:79], v[78:79], v[100:101]
	v_mov_b32_e32 v100, v70
	v_mov_b32_e32 v101, v72
	v_pk_mul_f32 v[102:103], v[102:103], v[102:103]
	v_pk_add_f32 v[42:43], v[42:43], v[110:111]
	v_pk_fma_f32 v[100:101], v[100:101], v[100:101], v[102:103]
	v_pk_fma_f32 v[102:103], v[66:67], v[66:67], v[80:81] op_sel_hi:[1,1,0]
	v_mul_f32_e32 v80, v69, v69
	v_pk_add_f32 v[78:79], v[78:79], v[78:79] op_sel:[0,1] op_sel_hi:[1,0]
	v_pk_add_f32 v[100:101], v[100:101], v[100:101] op_sel:[0,1] op_sel_hi:[1,0]
	v_pk_fma_f32 v[108:109], v[68:69], v[68:69], v[80:81] op_sel_hi:[1,1,0]
	v_pk_mul_f32 v[110:111], v[62:63], v[62:63]
	v_pk_mul_f32 v[112:113], v[64:65], v[64:65]
	v_mov_b32_e32 v79, v110
	v_mov_b32_e32 v101, v111
	v_mov_b32_e32 v103, v112
	v_mov_b32_e32 v109, v113
	v_pk_add_f32 v[78:79], v[78:79], v[100:101]
	v_pk_add_f32 v[100:101], v[102:103], v[108:109]
	v_mov_b32_e32 v102, v59
	v_mov_b32_e32 v103, v61
	v_pk_add_f32 v[78:79], v[78:79], v[100:101]
	v_mov_b32_e32 v100, v58
	v_mov_b32_e32 v101, v60
	v_pk_mul_f32 v[102:103], v[102:103], v[102:103]
	v_mul_f32_e32 v80, v47, v47
	v_pk_fma_f32 v[100:101], v[100:101], v[100:101], v[102:103]
	v_pk_fma_f32 v[102:103], v[46:47], v[46:47], v[80:81] op_sel_hi:[1,1,0]
	v_mul_f32_e32 v80, v49, v49
	v_pk_add_f32 v[78:79], v[78:79], v[78:79] op_sel:[0,1] op_sel_hi:[1,0]
	v_pk_add_f32 v[100:101], v[100:101], v[100:101] op_sel:[0,1] op_sel_hi:[1,0]
	v_pk_fma_f32 v[108:109], v[48:49], v[48:49], v[80:81] op_sel_hi:[1,1,0]
	v_pk_mul_f32 v[110:111], v[42:43], v[42:43]
	v_pk_mul_f32 v[112:113], v[44:45], v[44:45]
	v_mov_b32_e32 v79, v110
	v_mov_b32_e32 v101, v111
	v_mov_b32_e32 v103, v112
	v_mov_b32_e32 v109, v113
	v_pk_add_f32 v[78:79], v[78:79], v[100:101]
	v_pk_add_f32 v[100:101], v[102:103], v[108:109]
	s_nop 0
	v_pk_add_f32 v[78:79], v[78:79], v[100:101]
	s_nop 0
	v_add_f32_e32 v78, v78, v79
	ds_bpermute_b32 v79, v3, v78
	s_waitcnt lgkmcnt(0)
; #define GAS __attribute__((address_space(1)))
; __device__ __forceinline__ unsigned pk2(float lo, float hi) { f32x2_m v = {lo, hi}; bf16x2_m b = __builtin_convertvector(v, bf16x2_m); return __builtin_bit_cast(unsigned, b); }
; template <int MODE, bool W8 = false>
; __device__ __forceinline__ void norm_rows(const Ctx& C, const void* src, bf16* xdst, const unsigned char* YS8, const int* srow, const float* gate, const float* gain, bf16* XN, float* outf, unsigned char* XN8 = nullptr) {
;     ...
;             const float rstd = 1.0f / sqrtf(wave_sum(ss) * (1.0f / DM) + RMS_EPS);
;             if (MODE == 1) { GAS v2u* xo = (GAS v2u*)(xdst + (size_t)m * DM) + C.lane;
; #pragma unroll
;                 for (int j = 0; j < 8; ++j) { v2u w; w.x = pk2(v[q][j].x, v[q][j].y); w.y = pk2(v[q][j].z, v[q][j].w); xo[64 * j] = w; } }
;             const GAS f32x4* gg = (const GAS f32x4*)gain + C.lane;
;             if (MODE <= 1) { GAS v2u* o = (GAS v2u*)(XN + (size_t)m * DM) + C.lane;
; #pragma unroll
;                 for (int j = 0; j < 8; ++j) { const f32x4 g = gg[64 * j]; const f32x4 y = v[q][j] * rstd * g; v2u w; w.x = pk2(y.x, y.y); w.y = pk2(y.z, y.w); o[64 * j] = w;
;                     if constexpr (W8) ((GAS unsigned*)(XN8 + (size_t)m * DM) + C.lane)[64 * j] = pk4_fp8m(y.x * SXN, y.y * SXN, y.z * SXN, y.w * SXN); } }
	v_add_f32_e32 v78, v78, v79
	ds_bpermute_b32 v79, v57, v78
	s_waitcnt lgkmcnt(0)
	v_add_f32_e32 v78, v78, v79
	ds_bpermute_b32 v79, v81, v78
	s_waitcnt lgkmcnt(0)
	v_add_f32_e32 v78, v78, v79
	ds_bpermute_b32 v79, v82, v78
	s_waitcnt lgkmcnt(0)
	v_add_f32_e32 v78, v78, v79
	ds_bpermute_b32 v79, v83, v78
	s_waitcnt lgkmcnt(0)
	v_add_f32_e32 v78, v78, v79
	ds_bpermute_b32 v79, v84, v78
	s_waitcnt lgkmcnt(0)
	v_add_f32_e32 v78, v78, v79
	v_fmamk_f32 v78, v78, 0x3a000000, v212
	v_cmp_gt_f32_e32 vcc, s12, v78
	v_mul_f32_e32 v79, 0x4f800000, v78
	s_nop 0
	v_cndmask_b32_e32 v78, v78, v79, vcc
	v_sqrt_f32_e32 v79, v78
	s_nop 0
	v_add_u32_e32 v80, -1, v79
	v_fma_f32 v100, -v80, v79, v78
	v_cmp_ge_f32_e64 s[2:3], 0, v100
	v_add_u32_e32 v100, 1, v79
	s_nop 0
	v_cndmask_b32_e64 v80, v79, v80, s[2:3]
	v_fma_f32 v79, -v100, v79, v78
	v_cmp_lt_f32_e64 s[2:3], 0, v79
	s_nop 1
	v_cndmask_b32_e64 v79, v80, v100, s[2:3]
	v_mul_f32_e32 v80, 0x37800000, v79
	v_cndmask_b32_e32 v79, v79, v80, vcc
	v_cmp_class_f32_e32 vcc, v78, v211
	s_nop 1
	v_cndmask_b32_e32 v80, v79, v78, vcc
	v_cvt_pk_bf16_f32 v78, v104, v105
	v_cvt_pk_bf16_f32 v79, v106, v107
	global_store_dwordx2 v[50:51], v[78:79], off
	s_nop 1
	v_cvt_pk_bf16_f32 v78, v74, v75
	v_cvt_pk_bf16_f32 v79, v76, v77
	global_store_dwordx2 v[50:51], v[78:79], off offset:512
	s_nop 1
	v_cvt_pk_bf16_f32 v78, v70, v71
	v_cvt_pk_bf16_f32 v79, v72, v73
	global_store_dwordx2 v[50:51], v[78:79], off offset:1024
	s_nop 1
	v_cvt_pk_bf16_f32 v78, v66, v67
	v_cvt_pk_bf16_f32 v79, v68, v69
	global_store_dwordx2 v[50:51], v[78:79], off offset:1536
	s_nop 1
	v_cvt_pk_bf16_f32 v78, v62, v63
	v_cvt_pk_bf16_f32 v79, v64, v65
	global_store_dwordx2 v[50:51], v[78:79], off offset:2048
	s_nop 1
	v_cvt_pk_bf16_f32 v78, v58, v59
	v_cvt_pk_bf16_f32 v79, v60, v61
	global_store_dwordx2 v[50:51], v[78:79], off offset:2560
	s_nop 1
	v_cvt_pk_bf16_f32 v78, v46, v47
	v_cvt_pk_bf16_f32 v79, v48, v49
	global_store_dwordx2 v[50:51], v[78:79], off offset:3072
	s_nop 1
	v_cvt_pk_bf16_f32 v78, v42, v43
	v_cvt_pk_bf16_f32 v79, v44, v45
	global_store_dwordx2 v[50:51], v[78:79], off offset:3584
	s_nop 1
	v_div_scale_f32 v50, s[2:3], v80, v80, 1.0
	v_rcp_f32_e32 v51, v50
	s_nop 0
	v_fma_f32 v78, -v50, v51, 1.0
	v_fmac_f32_e32 v51, v78, v51
	v_div_scale_f32 v78, vcc, 1.0, v80, 1.0
	v_mul_f32_e32 v79, v78, v51
	v_fma_f32 v100, -v50, v79, v78
	v_fmac_f32_e32 v79, v100, v51
	v_fma_f32 v50, -v50, v79, v78
	v_div_fmas_f32 v50, v50, v51, v79
	v_div_fixup_f32 v50, v50, v80, 1.0
	v_pk_mul_f32 v[78:79], v[104:105], v[50:51] op_sel_hi:[1,0]
	v_pk_mul_f32 v[104:105], v[106:107], v[50:51] op_sel_hi:[1,0]
	v_add_co_u32_e32 v52, vcc, s16, v52
	v_pk_mul_f32 v[102:103], v[162:163], v[104:105]
	v_pk_mul_f32 v[78:79], v[160:161], v[78:79]
	v_cvt_pk_bf16_f32 v101, v102, v103
	v_cvt_pk_bf16_f32 v100, v78, v79
	v_addc_co_u32_e32 v53, vcc, 0, v53, vcc
	v_mul_f32_e32 v51, 0x42000000, v78
	v_mul_f32_e32 v78, 0x42000000, v79
	global_store_dwordx2 v[52:53], v[100:101], off
	s_nop 1
	v_med3_f32 v51, v51, s33, v214
	v_med3_f32 v78, v78, s33, v214
	v_mov_b32_e32 v100, v2
	v_cvt_pk_fp8_f32 v100, v51, v78
	v_mul_f32_e32 v79, 0x42000000, v102
	v_mul_f32_e32 v80, 0x42000000, v103
	v_med3_f32 v79, v79, s33, v214
	v_med3_f32 v80, v80, s33, v214
	v_cvt_pk_fp8_f32 v100, v79, v80 op_sel:[0,0,1]
	v_lshl_add_u64 v[78:79], s[4:5], 0, v[18:19]
	v_add_co_u32_e32 v78, vcc, s17, v78
	v_pk_mul_f32 v[74:75], v[74:75], v[50:51] op_sel_hi:[1,0]
	s_nop 0
	v_addc_co_u32_e32 v79, vcc, 0, v79, vcc
	global_store_dword v[78:79], v100, off
	s_nop 1
	v_pk_mul_f32 v[76:77], v[76:77], v[50:51] op_sel_hi:[1,0]
	v_lshl_add_u64 v[18:19], v[18:19], 0, s[18:19]
	v_pk_mul_f32 v[74:75], v[164:165], v[74:75]
	v_pk_mul_f32 v[76:77], v[166:167], v[76:77]
	v_cvt_pk_bf16_f32 v100, v74, v75
	v_mul_f32_e32 v51, 0x42000000, v74
	v_mul_f32_e32 v74, 0x42000000, v75
	v_cvt_pk_bf16_f32 v101, v76, v77
	v_mul_f32_e32 v75, 0x42000000, v76
	v_mul_f32_e32 v76, 0x42000000, v77
	v_med3_f32 v51, v51, s33, v214
	v_med3_f32 v74, v74, s33, v214
	v_mov_b32_e32 v77, v2
	v_cvt_pk_fp8_f32 v77, v51, v74
	v_med3_f32 v75, v75, s33, v214
	v_med3_f32 v76, v76, s33, v214
	global_store_dwordx2 v[52:53], v[100:101], off offset:512
	s_nop 1
	v_cvt_pk_fp8_f32 v77, v75, v76 op_sel:[0,0,1]
	v_pk_mul_f32 v[70:71], v[70:71], v[50:51] op_sel_hi:[1,0]
	v_pk_mul_f32 v[72:73], v[72:73], v[50:51] op_sel_hi:[1,0]
	global_store_dword v[78:79], v77, off offset:256
	s_nop 1
	v_pk_mul_f32 v[70:71], v[70:71], v[168:169]
	v_pk_mul_f32 v[72:73], v[72:73], v[170:171]
	v_cvt_pk_bf16_f32 v74, v70, v71
	v_mul_f32_e32 v51, 0x42000000, v70
	v_mul_f32_e32 v70, 0x42000000, v71
	v_cvt_pk_bf16_f32 v75, v72, v73
	v_mul_f32_e32 v71, 0x42000000, v72
	v_mul_f32_e32 v72, 0x42000000, v73
	v_med3_f32 v51, v51, s33, v214
	v_med3_f32 v70, v70, s33, v214
	v_mov_b32_e32 v73, v2
	v_cvt_pk_fp8_f32 v73, v51, v70
	v_med3_f32 v71, v71, s33, v214
	v_med3_f32 v72, v72, s33, v214
	global_store_dwordx2 v[52:53], v[74:75], off offset:1024
	s_nop 1
	v_cvt_pk_fp8_f32 v73, v71, v72 op_sel:[0,0,1]
	v_pk_mul_f32 v[66:67], v[66:67], v[50:51] op_sel_hi:[1,0]
	v_pk_mul_f32 v[68:69], v[68:69], v[50:51] op_sel_hi:[1,0]
	global_store_dword v[78:79], v73, off offset:512
	s_nop 1
	v_pk_mul_f32 v[66:67], v[66:67], v[172:173]
	v_pk_mul_f32 v[68:69], v[68:69], v[174:175]
	v_cvt_pk_bf16_f32 v70, v66, v67
	v_mul_f32_e32 v51, 0x42000000, v66
	v_mul_f32_e32 v66, 0x42000000, v67
	v_cvt_pk_bf16_f32 v71, v68, v69
	v_mul_f32_e32 v67, 0x42000000, v68
	v_mul_f32_e32 v68, 0x42000000, v69
	v_med3_f32 v51, v51, s33, v214
	v_med3_f32 v66, v66, s33, v214
	v_mov_b32_e32 v69, v2
	v_cvt_pk_fp8_f32 v69, v51, v66
	v_med3_f32 v67, v67, s33, v214
; #define GAS __attribute__((address_space(1)))
; __device__ __forceinline__ unsigned pk2(float lo, float hi) { f32x2_m v = {lo, hi}; bf16x2_m b = __builtin_convertvector(v, bf16x2_m); return __builtin_bit_cast(unsigned, b); }
; template <int MODE, bool W8 = false>
; __device__ __forceinline__ void norm_rows(const Ctx& C, const void* src, bf16* xdst, const unsigned char* YS8, const int* srow, const float* gate, const float* gain, bf16* XN, float* outf, unsigned char* XN8 = nullptr) {
;     ...
;                 for (int j = 0; j < 8; ++j) { const unsigned a = ya[q][j], b = yb[q][j];
;                     const f32x2_m a01 = __builtin_amdgcn_cvt_pk_f32_fp8((int)a, false), a23 = __builtin_amdgcn_cvt_pk_f32_fp8((int)a, true), b01 = __builtin_amdgcn_cvt_pk_f32_fp8((int)b, false), b23 = __builtin_amdgcn_cvt_pk_f32_fp8((int)b, true);
;                     v[q][j].x += h0[q] * a01.x + h1[q] * b01.x; v[q][j].y += h0[q] * a01.y + h1[q] * b01.y; v[q][j].z += h0[q] * a23.x + h1[q] * b23.x; v[q][j].w += h0[q] * a23.y + h1[q] * b23.y; } }
;     ...
;             if (MODE <= 1) { GAS v2u* o = (GAS v2u*)(XN + (size_t)m * DM) + C.lane;
; #pragma unroll
;                 for (int j = 0; j < 8; ++j) { const f32x4 g = gg[64 * j]; const f32x4 y = v[q][j] * rstd * g; v2u w; w.x = pk2(y.x, y.y); w.y = pk2(y.z, y.w); o[64 * j] = w;
;                     if constexpr (W8) ((GAS unsigned*)(XN8 + (size_t)m * DM) + C.lane)[64 * j] = pk4_fp8m(y.x * SXN, y.y * SXN, y.z * SXN, y.w * SXN); } }
	v_med3_f32 v68, v68, s33, v214
	global_store_dwordx2 v[52:53], v[70:71], off offset:1536
	s_nop 1
	v_cvt_pk_fp8_f32 v69, v67, v68 op_sel:[0,0,1]
	v_pk_mul_f32 v[62:63], v[62:63], v[50:51] op_sel_hi:[1,0]
	v_pk_mul_f32 v[64:65], v[64:65], v[50:51] op_sel_hi:[1,0]
	global_store_dword v[78:79], v69, off offset:768
	s_nop 1
	v_pk_mul_f32 v[62:63], v[62:63], v[176:177]
	v_pk_mul_f32 v[64:65], v[64:65], v[178:179]
	v_cvt_pk_bf16_f32 v66, v62, v63
	v_mul_f32_e32 v51, 0x42000000, v62
	v_mul_f32_e32 v62, 0x42000000, v63
	v_cvt_pk_bf16_f32 v67, v64, v65
	v_mul_f32_e32 v63, 0x42000000, v64
	v_mul_f32_e32 v64, 0x42000000, v65
	v_med3_f32 v51, v51, s33, v214
	v_med3_f32 v62, v62, s33, v214
	v_mov_b32_e32 v65, v2
	v_cvt_pk_fp8_f32 v65, v51, v62
	v_med3_f32 v63, v63, s33, v214
	v_med3_f32 v64, v64, s33, v214
	global_store_dwordx2 v[52:53], v[66:67], off offset:2048
	s_nop 1
	v_cvt_pk_fp8_f32 v65, v63, v64 op_sel:[0,0,1]
	v_pk_mul_f32 v[58:59], v[58:59], v[50:51] op_sel_hi:[1,0]
	v_pk_mul_f32 v[60:61], v[60:61], v[50:51] op_sel_hi:[1,0]
	v_lshlrev_b32_e32 v66, 16, v22
	global_store_dword v[78:79], v65, off offset:1024
	s_nop 1
	v_and_b32_e32 v67, 0xffff0000, v22
	v_lshlrev_b32_e32 v22, 16, v23
	v_and_b32_e32 v23, 0xffff0000, v23
	v_lshlrev_b32_e32 v68, 16, v24
	v_and_b32_e32 v69, 0xffff0000, v24
	v_lshlrev_b32_e32 v24, 16, v25
	v_and_b32_e32 v25, 0xffff0000, v25
	v_pk_mul_f32 v[58:59], v[58:59], v[180:181]
	v_pk_mul_f32 v[60:61], v[60:61], v[182:183]
	v_cvt_pk_bf16_f32 v62, v58, v59
	v_mul_f32_e32 v51, 0x42000000, v58
	v_mul_f32_e32 v58, 0x42000000, v59
	v_cvt_pk_bf16_f32 v63, v60, v61
	v_mul_f32_e32 v59, 0x42000000, v60
	v_mul_f32_e32 v60, 0x42000000, v61
	v_med3_f32 v51, v51, s33, v214
	v_med3_f32 v58, v58, s33, v214
	v_mov_b32_e32 v61, v2
	v_cvt_pk_fp8_f32 v61, v51, v58
	v_med3_f32 v59, v59, s33, v214
	v_med3_f32 v60, v60, s33, v214
	global_store_dwordx2 v[52:53], v[62:63], off offset:2560
	s_nop 1
	v_cvt_pk_fp8_f32 v61, v59, v60 op_sel:[0,0,1]
	v_pk_mul_f32 v[46:47], v[46:47], v[50:51] op_sel_hi:[1,0]
	v_pk_mul_f32 v[48:49], v[48:49], v[50:51] op_sel_hi:[1,0]
	v_mov_b32_e32 v51, v2
	global_store_dword v[78:79], v61, off offset:1280
	s_nop 1
	v_pk_mul_f32 v[46:47], v[46:47], v[184:185]
	s_nop 0
	v_cvt_pk_bf16_f32 v58, v46, v47
	v_mul_f32_e32 v46, 0x42000000, v46
	v_mul_f32_e32 v47, 0x42000000, v47
	v_med3_f32 v46, v46, s33, v214
	v_med3_f32 v47, v47, s33, v214
	v_cvt_pk_fp8_f32 v51, v46, v47
	v_pk_mul_f32 v[48:49], v[48:49], v[186:187]
	v_lshlrev_b32_e32 v60, 16, v30
	v_cvt_pk_bf16_f32 v59, v48, v49
	v_mul_f32_e32 v48, 0x42000000, v48
	v_mul_f32_e32 v49, 0x42000000, v49
	v_med3_f32 v48, v48, s33, v214
	v_med3_f32 v49, v49, s33, v214
	v_cvt_pk_fp8_f32 v51, v48, v49 op_sel:[0,0,1]
	global_store_dwordx2 v[52:53], v[58:59], off offset:3072
	s_nop 1
	v_lshlrev_b32_e32 v58, 16, v32
	v_and_b32_e32 v59, 0xffff0000, v32
	global_store_dword v[78:79], v51, off offset:1536
	s_nop 1
	v_pk_mul_f32 v[42:43], v[42:43], v[50:51] op_sel_hi:[1,0]
	v_pk_mul_f32 v[44:45], v[44:45], v[50:51] op_sel_hi:[1,0]
	v_lshlrev_b32_e32 v50, 16, v40
	v_and_b32_e32 v51, 0xffff0000, v40
	v_lshlrev_b32_e32 v40, 16, v41
	v_and_b32_e32 v41, 0xffff0000, v41
	v_lshlrev_b32_e32 v32, 16, v33
	v_and_b32_e32 v33, 0xffff0000, v33
	v_and_b32_e32 v61, 0xffff0000, v30
	v_lshlrev_b32_e32 v30, 16, v31
	v_and_b32_e32 v31, 0xffff0000, v31
	v_pk_mul_f32 v[44:45], v[44:45], v[190:191]
	v_pk_mul_f32 v[42:43], v[42:43], v[188:189]
	v_cvt_pk_bf16_f32 v47, v44, v45
	v_cvt_pk_bf16_f32 v46, v42, v43
	v_mul_f32_e32 v42, 0x42000000, v42
	v_mul_f32_e32 v43, 0x42000000, v43
	global_store_dwordx2 v[52:53], v[46:47], off offset:3584
	s_nop 1
	v_med3_f32 v42, v42, s33, v214
	v_med3_f32 v43, v43, s33, v214
	v_mov_b32_e32 v46, v2
	v_cvt_pk_fp8_f32 v46, v42, v43
	v_mul_f32_e32 v44, 0x42000000, v44
	v_mul_f32_e32 v45, 0x42000000, v45
	v_med3_f32 v44, v44, s33, v214
	v_med3_f32 v45, v45, s33, v214
	v_cvt_pk_fp8_f32 v46, v44, v45 op_sel:[0,0,1]
	s_waitcnt vmcnt(23)
	v_cvt_pk_f32_fp8_e32 v[42:43], v99
	v_cvt_pk_f32_fp8_sdwa v[48:49], v98 src0_sel:WORD_1
	v_cvt_pk_f32_fp8_sdwa v[44:45], v99 src0_sel:WORD_1
	global_store_dword v[78:79], v46, off offset:1792
	s_nop 1
	v_cvt_pk_f32_fp8_e32 v[46:47], v98
	v_pk_mul_f32 v[46:47], v[56:57], v[46:47] op_sel_hi:[0,1]
	v_pk_fma_f32 v[42:43], v[54:55], v[42:43], v[46:47] op_sel_hi:[0,1,1]
	v_pk_add_f32 v[62:63], v[42:43], v[50:51]
	v_pk_mul_f32 v[42:43], v[56:57], v[48:49] op_sel_hi:[0,1]
	v_pk_fma_f32 v[42:43], v[54:55], v[44:45], v[42:43] op_sel_hi:[0,1,1]
	v_cvt_pk_f32_fp8_e32 v[44:45], v96
	v_pk_add_f32 v[64:65], v[42:43], v[40:41]
	v_cvt_pk_f32_fp8_e32 v[40:41], v97
	v_cvt_pk_f32_fp8_sdwa v[46:47], v96 src0_sel:WORD_1
	v_cvt_pk_f32_fp8_sdwa v[42:43], v97 src0_sel:WORD_1
	v_pk_mul_f32 v[44:45], v[56:57], v[44:45] op_sel_hi:[0,1]
	v_lshlrev_b32_e32 v48, 16, v38
	v_and_b32_e32 v49, 0xffff0000, v38
	v_pk_fma_f32 v[40:41], v[54:55], v[40:41], v[44:45] op_sel_hi:[0,1,1]
	v_pk_add_f32 v[50:51], v[40:41], v[48:49]
	v_pk_mul_f32 v[40:41], v[56:57], v[46:47] op_sel_hi:[0,1]
	v_lshlrev_b32_e32 v38, 16, v39
	v_and_b32_e32 v39, 0xffff0000, v39
	v_pk_fma_f32 v[40:41], v[54:55], v[42:43], v[40:41] op_sel_hi:[0,1,1]
	v_cvt_pk_f32_fp8_e32 v[42:43], v94
	v_pk_add_f32 v[52:53], v[40:41], v[38:39]
	v_cvt_pk_f32_fp8_e32 v[38:39], v95
	v_cvt_pk_f32_fp8_sdwa v[44:45], v94 src0_sel:WORD_1
	v_cvt_pk_f32_fp8_sdwa v[40:41], v95 src0_sel:WORD_1
	v_pk_mul_f32 v[42:43], v[56:57], v[42:43] op_sel_hi:[0,1]
	v_lshlrev_b32_e32 v46, 16, v36
	v_and_b32_e32 v47, 0xffff0000, v36
	v_pk_fma_f32 v[38:39], v[54:55], v[38:39], v[42:43] op_sel_hi:[0,1,1]
	v_pk_add_f32 v[46:47], v[38:39], v[46:47]
; template <int MODE, bool W8 = false>
; __device__ __forceinline__ void norm_rows(const Ctx& C, const void* src, bf16* xdst, const unsigned char* YS8, const int* srow, const float* gate, const float* gain, bf16* XN, float* outf, unsigned char* XN8 = nullptr) {
;     ...
;                 for (int j = 0; j < 8; ++j) { const unsigned a = ya[q][j], b = yb[q][j];
;                     const f32x2_m a01 = __builtin_amdgcn_cvt_pk_f32_fp8((int)a, false), a23 = __builtin_amdgcn_cvt_pk_f32_fp8((int)a, true), b01 = __builtin_amdgcn_cvt_pk_f32_fp8((int)b, false), b23 = __builtin_amdgcn_cvt_pk_f32_fp8((int)b, true);
;                     v[q][j].x += h0[q] * a01.x + h1[q] * b01.x; v[q][j].y += h0[q] * a01.y + h1[q] * b01.y; v[q][j].z += h0[q] * a23.x + h1[q] * b23.x; v[q][j].w += h0[q] * a23.y + h1[q] * b23.y; } }
;             float ss = 0.f;
; #pragma unroll
;             for (int j = 0; j < 8; ++j) ss += (v[q][j].x * v[q][j].x + v[q][j].y * v[q][j].y) + (v[q][j].z * v[q][j].z + v[q][j].w * v[q][j].w);
;             const float rstd = 1.0f / sqrtf(wave_sum(ss) * (1.0f / DM) + RMS_EPS);
	v_pk_mul_f32 v[38:39], v[56:57], v[44:45] op_sel_hi:[0,1]
	v_lshlrev_b32_e32 v36, 16, v37
	v_and_b32_e32 v37, 0xffff0000, v37
	v_pk_fma_f32 v[38:39], v[54:55], v[40:41], v[38:39] op_sel_hi:[0,1,1]
	v_cvt_pk_f32_fp8_e32 v[40:41], v92
	v_pk_add_f32 v[48:49], v[38:39], v[36:37]
	v_cvt_pk_f32_fp8_e32 v[36:37], v93
	v_cvt_pk_f32_fp8_sdwa v[44:45], v92 src0_sel:WORD_1
	v_cvt_pk_f32_fp8_sdwa v[38:39], v93 src0_sel:WORD_1
	v_pk_mul_f32 v[40:41], v[56:57], v[40:41] op_sel_hi:[0,1]
	v_lshlrev_b32_e32 v42, 16, v34
	v_and_b32_e32 v43, 0xffff0000, v34
	v_pk_fma_f32 v[36:37], v[54:55], v[36:37], v[40:41] op_sel_hi:[0,1,1]
	v_pk_add_f32 v[42:43], v[36:37], v[42:43]
	v_pk_mul_f32 v[36:37], v[56:57], v[44:45] op_sel_hi:[0,1]
	v_lshlrev_b32_e32 v34, 16, v35
	v_and_b32_e32 v35, 0xffff0000, v35
	v_pk_fma_f32 v[36:37], v[54:55], v[38:39], v[36:37] op_sel_hi:[0,1,1]
	v_cvt_pk_f32_fp8_e32 v[38:39], v90
	v_pk_add_f32 v[44:45], v[36:37], v[34:35]
	v_cvt_pk_f32_fp8_e32 v[34:35], v91
	v_cvt_pk_f32_fp8_sdwa v[40:41], v90 src0_sel:WORD_1
	v_cvt_pk_f32_fp8_sdwa v[36:37], v91 src0_sel:WORD_1
	v_pk_mul_f32 v[38:39], v[56:57], v[38:39] op_sel_hi:[0,1]
	v_pk_fma_f32 v[34:35], v[54:55], v[34:35], v[38:39] op_sel_hi:[0,1,1]
	v_pk_add_f32 v[38:39], v[34:35], v[58:59]
	v_pk_mul_f32 v[34:35], v[56:57], v[40:41] op_sel_hi:[0,1]
	v_pk_fma_f32 v[34:35], v[54:55], v[36:37], v[34:35] op_sel_hi:[0,1,1]
	v_pk_add_f32 v[40:41], v[34:35], v[32:33]
	v_cvt_pk_f32_fp8_e32 v[34:35], v88
	v_cvt_pk_f32_fp8_e32 v[32:33], v89
	v_cvt_pk_f32_fp8_sdwa v[58:59], v88 src0_sel:WORD_1
	v_cvt_pk_f32_fp8_sdwa v[36:37], v89 src0_sel:WORD_1
	v_pk_mul_f32 v[34:35], v[56:57], v[34:35] op_sel_hi:[0,1]
	v_pk_fma_f32 v[32:33], v[54:55], v[32:33], v[34:35] op_sel_hi:[0,1,1]
	v_pk_add_f32 v[34:35], v[32:33], v[60:61]
	v_pk_mul_f32 v[32:33], v[56:57], v[58:59] op_sel_hi:[0,1]
	v_pk_fma_f32 v[32:33], v[54:55], v[36:37], v[32:33] op_sel_hi:[0,1,1]
	v_cvt_pk_f32_fp8_e32 v[58:59], v86
	v_pk_add_f32 v[36:37], v[32:33], v[30:31]
	v_cvt_pk_f32_fp8_e32 v[30:31], v87
	v_cvt_pk_f32_fp8_sdwa v[60:61], v86 src0_sel:WORD_1
	v_cvt_pk_f32_fp8_sdwa v[32:33], v87 src0_sel:WORD_1
	v_pk_mul_f32 v[58:59], v[56:57], v[58:59] op_sel_hi:[0,1]
	v_pk_fma_f32 v[30:31], v[54:55], v[30:31], v[58:59] op_sel_hi:[0,1,1]
	v_pk_mul_f32 v[58:59], v[56:57], v[60:61] op_sel_hi:[0,1]
	v_pk_fma_f32 v[32:33], v[54:55], v[32:33], v[58:59] op_sel_hi:[0,1,1]
	v_cvt_pk_f32_fp8_e32 v[60:61], v55
	v_pk_add_f32 v[30:31], v[30:31], v[66:67]
	v_pk_add_f32 v[32:33], v[32:33], v[22:23]
	v_cvt_pk_f32_fp8_e32 v[22:23], v85
	v_cvt_pk_f32_fp8_sdwa v[66:67], v55 src0_sel:WORD_1
	v_cvt_pk_f32_fp8_sdwa v[58:59], v85 src0_sel:WORD_1
	v_pk_mul_f32 v[60:61], v[56:57], v[60:61] op_sel_hi:[0,1]
	v_pk_fma_f32 v[22:23], v[54:55], v[22:23], v[60:61] op_sel_hi:[0,1,1]
	v_pk_mul_f32 v[60:61], v[56:57], v[66:67] op_sel_hi:[0,1]
	v_pk_fma_f32 v[54:55], v[54:55], v[58:59], v[60:61] op_sel_hi:[0,1,1]
	v_mov_b32_e32 v58, v63
	v_mov_b32_e32 v59, v51
	v_pk_add_f32 v[24:25], v[54:55], v[24:25]
	v_mov_b32_e32 v54, v62
	v_mov_b32_e32 v55, v50
	v_pk_mul_f32 v[58:59], v[58:59], v[58:59]
	v_mov_b32_e32 v60, v65
	v_mov_b32_e32 v61, v53
	v_pk_fma_f32 v[54:55], v[54:55], v[54:55], v[58:59]
	v_mov_b32_e32 v58, v64
	v_mov_b32_e32 v59, v52
	v_pk_mul_f32 v[60:61], v[60:61], v[60:61]
	v_mul_f32_e32 v56, v43, v43
	v_pk_fma_f32 v[58:59], v[58:59], v[58:59], v[60:61]
	v_mov_b32_e32 v60, v47
	v_mov_b32_e32 v61, v49
	v_pk_add_f32 v[54:55], v[54:55], v[58:59]
	v_mov_b32_e32 v58, v46
	v_mov_b32_e32 v59, v48
	v_pk_mul_f32 v[60:61], v[60:61], v[60:61]
	v_pk_add_f32 v[22:23], v[22:23], v[68:69]
	v_pk_fma_f32 v[58:59], v[58:59], v[58:59], v[60:61]
	v_pk_fma_f32 v[60:61], v[42:43], v[42:43], v[56:57] op_sel_hi:[1,1,0]
	v_mul_f32_e32 v56, v45, v45
	v_pk_add_f32 v[54:55], v[54:55], v[54:55] op_sel:[0,1] op_sel_hi:[1,0]
	v_pk_add_f32 v[58:59], v[58:59], v[58:59] op_sel:[0,1] op_sel_hi:[1,0]
	v_pk_fma_f32 v[66:67], v[44:45], v[44:45], v[56:57] op_sel_hi:[1,1,0]
	v_pk_mul_f32 v[68:69], v[38:39], v[38:39]
	v_pk_mul_f32 v[70:71], v[40:41], v[40:41]
	v_mov_b32_e32 v55, v68
	v_mov_b32_e32 v59, v69
	v_mov_b32_e32 v61, v70
	v_mov_b32_e32 v67, v71
	v_pk_add_f32 v[54:55], v[54:55], v[58:59]
	v_pk_add_f32 v[58:59], v[60:61], v[66:67]
	v_mov_b32_e32 v60, v35
	v_mov_b32_e32 v61, v37
	v_pk_add_f32 v[54:55], v[54:55], v[58:59]
	v_mov_b32_e32 v58, v34
	v_mov_b32_e32 v59, v36
	v_pk_mul_f32 v[60:61], v[60:61], v[60:61]
	v_mul_f32_e32 v56, v31, v31
	v_pk_fma_f32 v[58:59], v[58:59], v[58:59], v[60:61]
	v_pk_fma_f32 v[60:61], v[30:31], v[30:31], v[56:57] op_sel_hi:[1,1,0]
	v_mul_f32_e32 v56, v33, v33
	v_pk_add_f32 v[54:55], v[54:55], v[54:55] op_sel:[0,1] op_sel_hi:[1,0]
	v_pk_add_f32 v[58:59], v[58:59], v[58:59] op_sel:[0,1] op_sel_hi:[1,0]
	v_pk_fma_f32 v[66:67], v[32:33], v[32:33], v[56:57] op_sel_hi:[1,1,0]
	v_pk_mul_f32 v[68:69], v[22:23], v[22:23]
	v_pk_mul_f32 v[70:71], v[24:25], v[24:25]
	v_mov_b32_e32 v55, v68
	v_mov_b32_e32 v59, v69
	v_mov_b32_e32 v61, v70
	v_mov_b32_e32 v67, v71
	v_pk_add_f32 v[54:55], v[54:55], v[58:59]
	v_pk_add_f32 v[58:59], v[60:61], v[66:67]
	s_nop 0
	v_pk_add_f32 v[54:55], v[54:55], v[58:59]
	s_nop 0
	v_add_f32_e32 v54, v54, v55
	ds_bpermute_b32 v55, v3, v54
	s_waitcnt lgkmcnt(0)
	v_add_f32_e32 v54, v54, v55
	ds_bpermute_b32 v55, v57, v54
	s_waitcnt lgkmcnt(0)
	v_add_f32_e32 v54, v54, v55
	ds_bpermute_b32 v55, v81, v54
	s_waitcnt lgkmcnt(0)
	v_add_f32_e32 v54, v54, v55
	ds_bpermute_b32 v55, v82, v54
	s_waitcnt lgkmcnt(0)
	v_add_f32_e32 v54, v54, v55
	ds_bpermute_b32 v55, v83, v54
	s_waitcnt lgkmcnt(0)
	v_add_f32_e32 v54, v54, v55
	ds_bpermute_b32 v55, v84, v54
	s_waitcnt lgkmcnt(0)
; #define GAS __attribute__((address_space(1)))
; __device__ __forceinline__ unsigned pk2(float lo, float hi) { f32x2_m v = {lo, hi}; bf16x2_m b = __builtin_convertvector(v, bf16x2_m); return __builtin_bit_cast(unsigned, b); }
; template <int MODE, bool W8 = false>
; __device__ __forceinline__ void norm_rows(const Ctx& C, const void* src, bf16* xdst, const unsigned char* YS8, const int* srow, const float* gate, const float* gain, bf16* XN, float* outf, unsigned char* XN8 = nullptr) {
;     ...
;             const float rstd = 1.0f / sqrtf(wave_sum(ss) * (1.0f / DM) + RMS_EPS);
;             if (MODE == 1) { GAS v2u* xo = (GAS v2u*)(xdst + (size_t)m * DM) + C.lane;
; #pragma unroll
;                 for (int j = 0; j < 8; ++j) { v2u w; w.x = pk2(v[q][j].x, v[q][j].y); w.y = pk2(v[q][j].z, v[q][j].w); xo[64 * j] = w; } }
;             const GAS f32x4* gg = (const GAS f32x4*)gain + C.lane;
;             if (MODE <= 1) { GAS v2u* o = (GAS v2u*)(XN + (size_t)m * DM) + C.lane;
; #pragma unroll
;                 for (int j = 0; j < 8; ++j) { const f32x4 g = gg[64 * j]; const f32x4 y = v[q][j] * rstd * g; v2u w; w.x = pk2(y.x, y.y); w.y = pk2(y.z, y.w); o[64 * j] = w;
;                     if constexpr (W8) ((GAS unsigned*)(XN8 + (size_t)m * DM) + C.lane)[64 * j] = pk4_fp8m(y.x * SXN, y.y * SXN, y.z * SXN, y.w * SXN); } }
	v_add_f32_e32 v54, v54, v55
	v_fmamk_f32 v54, v54, 0x3a000000, v212
	v_cmp_gt_f32_e32 vcc, s12, v54
	v_mul_f32_e32 v55, 0x4f800000, v54
	s_nop 0
	v_cndmask_b32_e32 v54, v54, v55, vcc
	v_sqrt_f32_e32 v55, v54
	s_nop 0
	v_add_u32_e32 v56, -1, v55
	v_fma_f32 v58, -v56, v55, v54
	v_cmp_ge_f32_e64 s[2:3], 0, v58
	v_add_u32_e32 v58, 1, v55
	s_nop 0
	v_cndmask_b32_e64 v56, v55, v56, s[2:3]
	v_fma_f32 v55, -v58, v55, v54
	v_cmp_lt_f32_e64 s[2:3], 0, v55
	s_nop 1
	v_cndmask_b32_e64 v55, v56, v58, s[2:3]
	v_mul_f32_e32 v56, 0x37800000, v55
	v_cndmask_b32_e32 v55, v55, v56, vcc
	v_cmp_class_f32_e32 vcc, v54, v211
	s_nop 1
	v_cndmask_b32_e32 v56, v55, v54, vcc
	v_cvt_pk_bf16_f32 v54, v62, v63
	v_cvt_pk_bf16_f32 v55, v64, v65
	global_store_dwordx2 v[26:27], v[54:55], off
	s_nop 1
	v_cvt_pk_bf16_f32 v54, v50, v51
	v_cvt_pk_bf16_f32 v55, v52, v53
	global_store_dwordx2 v[26:27], v[54:55], off offset:512
	s_nop 1
	v_cvt_pk_bf16_f32 v54, v46, v47
	v_cvt_pk_bf16_f32 v55, v48, v49
	global_store_dwordx2 v[26:27], v[54:55], off offset:1024
	s_nop 1
	v_cvt_pk_bf16_f32 v54, v42, v43
	v_cvt_pk_bf16_f32 v55, v44, v45
	global_store_dwordx2 v[26:27], v[54:55], off offset:1536
	s_nop 1
	v_cvt_pk_bf16_f32 v54, v38, v39
	v_cvt_pk_bf16_f32 v55, v40, v41
	global_store_dwordx2 v[26:27], v[54:55], off offset:2048
	s_nop 1
	v_cvt_pk_bf16_f32 v54, v34, v35
	v_cvt_pk_bf16_f32 v55, v36, v37
	global_store_dwordx2 v[26:27], v[54:55], off offset:2560
	s_nop 1
	v_cvt_pk_bf16_f32 v54, v30, v31
	v_cvt_pk_bf16_f32 v55, v32, v33
	global_store_dwordx2 v[26:27], v[54:55], off offset:3072
	s_nop 1
	v_cvt_pk_bf16_f32 v54, v22, v23
	v_cvt_pk_bf16_f32 v55, v24, v25
	global_store_dwordx2 v[26:27], v[54:55], off offset:3584
	s_nop 1
	v_div_scale_f32 v26, s[2:3], v56, v56, 1.0
	v_rcp_f32_e32 v27, v26
	s_nop 0
	v_fma_f32 v54, -v26, v27, 1.0
	v_fmac_f32_e32 v27, v54, v27
	v_div_scale_f32 v54, vcc, 1.0, v56, 1.0
	v_mul_f32_e32 v55, v54, v27
	v_fma_f32 v58, -v26, v55, v54
	v_fmac_f32_e32 v55, v58, v27
	v_fma_f32 v26, -v26, v55, v54
	v_div_fmas_f32 v26, v26, v27, v55
	v_div_fixup_f32 v26, v26, v56, 1.0
	v_pk_mul_f32 v[54:55], v[62:63], v[26:27] op_sel_hi:[1,0]
	v_pk_mul_f32 v[62:63], v[64:65], v[26:27] op_sel_hi:[1,0]
	v_add_co_u32_e32 v28, vcc, s16, v28
	v_pk_mul_f32 v[54:55], v[160:161], v[54:55]
	s_nop 0
	v_cvt_pk_bf16_f32 v58, v54, v55
	v_mul_f32_e32 v27, 0x42000000, v54
	v_mul_f32_e32 v55, 0x42000000, v55
	v_med3_f32 v54, v27, s33, v214
	v_med3_f32 v55, v55, s33, v214
	v_mov_b32_e32 v27, v2
	v_pk_mul_f32 v[60:61], v[162:163], v[62:63]
	v_cvt_pk_fp8_f32 v27, v54, v55
	v_cvt_pk_bf16_f32 v59, v60, v61
	v_addc_co_u32_e32 v29, vcc, 0, v29, vcc
	global_store_dwordx2 v[28:29], v[58:59], off
	s_nop 1
	v_mul_f32_e32 v56, 0x42000000, v60
	v_mul_f32_e32 v58, 0x42000000, v61
	v_med3_f32 v56, v56, s33, v214
	v_med3_f32 v58, v58, s33, v214
	v_cvt_pk_fp8_f32 v27, v56, v58 op_sel:[0,0,1]
	v_lshl_add_u64 v[54:55], s[4:5], 0, v[14:15]
	v_add_co_u32_e32 v54, vcc, s17, v54
	v_pk_mul_f32 v[50:51], v[50:51], v[26:27] op_sel_hi:[1,0]
	s_nop 0
	v_addc_co_u32_e32 v55, vcc, 0, v55, vcc
	global_store_dword v[54:55], v27, off
	s_nop 1
	v_pk_mul_f32 v[52:53], v[52:53], v[26:27] op_sel_hi:[1,0]
	v_lshl_add_u64 v[14:15], v[14:15], 0, s[18:19]
	v_pk_mul_f32 v[50:51], v[164:165], v[50:51]
	v_pk_mul_f32 v[52:53], v[166:167], v[52:53]
	v_cvt_pk_bf16_f32 v58, v50, v51
	v_mul_f32_e32 v27, 0x42000000, v50
	v_mul_f32_e32 v50, 0x42000000, v51
	v_cvt_pk_bf16_f32 v59, v52, v53
	v_mul_f32_e32 v51, 0x42000000, v52
	v_mul_f32_e32 v52, 0x42000000, v53
	v_med3_f32 v27, v27, s33, v214
	v_med3_f32 v50, v50, s33, v214
	v_mov_b32_e32 v53, v2
	v_cvt_pk_fp8_f32 v53, v27, v50
	v_med3_f32 v51, v51, s33, v214
	v_med3_f32 v52, v52, s33, v214
	global_store_dwordx2 v[28:29], v[58:59], off offset:512
	s_nop 1
	v_cvt_pk_fp8_f32 v53, v51, v52 op_sel:[0,0,1]
	v_pk_mul_f32 v[46:47], v[46:47], v[26:27] op_sel_hi:[1,0]
	v_pk_mul_f32 v[48:49], v[48:49], v[26:27] op_sel_hi:[1,0]
	global_store_dword v[54:55], v53, off offset:256
	s_nop 1
	v_pk_mul_f32 v[46:47], v[46:47], v[168:169]
	v_pk_mul_f32 v[48:49], v[48:49], v[170:171]
	v_cvt_pk_bf16_f32 v50, v46, v47
	v_mul_f32_e32 v27, 0x42000000, v46
	v_mul_f32_e32 v46, 0x42000000, v47
	v_cvt_pk_bf16_f32 v51, v48, v49
	v_mul_f32_e32 v47, 0x42000000, v48
	v_mul_f32_e32 v48, 0x42000000, v49
; #define GAS __attribute__((address_space(1)))
; __device__ __forceinline__ unsigned pk2(float lo, float hi) { f32x2_m v = {lo, hi}; bf16x2_m b = __builtin_convertvector(v, bf16x2_m); return __builtin_bit_cast(unsigned, b); }
; template <int MODE, bool W8 = false>
; __device__ __forceinline__ void norm_rows(const Ctx& C, const void* src, bf16* xdst, const unsigned char* YS8, const int* srow, const float* gate, const float* gain, bf16* XN, float* outf, unsigned char* XN8 = nullptr) {
;     ...
;             if (MODE <= 1) { GAS v2u* o = (GAS v2u*)(XN + (size_t)m * DM) + C.lane;
; #pragma unroll
;                 for (int j = 0; j < 8; ++j) { const f32x4 g = gg[64 * j]; const f32x4 y = v[q][j] * rstd * g; v2u w; w.x = pk2(y.x, y.y); w.y = pk2(y.z, y.w); o[64 * j] = w;
;                     if constexpr (W8) ((GAS unsigned*)(XN8 + (size_t)m * DM) + C.lane)[64 * j] = pk4_fp8m(y.x * SXN, y.y * SXN, y.z * SXN, y.w * SXN); } }
	v_med3_f32 v27, v27, s33, v214
	v_med3_f32 v46, v46, s33, v214
	v_mov_b32_e32 v49, v2
	v_cvt_pk_fp8_f32 v49, v27, v46
	v_med3_f32 v47, v47, s33, v214
	v_med3_f32 v48, v48, s33, v214
	global_store_dwordx2 v[28:29], v[50:51], off offset:1024
	s_nop 1
	v_cvt_pk_fp8_f32 v49, v47, v48 op_sel:[0,0,1]
	v_pk_mul_f32 v[42:43], v[42:43], v[26:27] op_sel_hi:[1,0]
	v_pk_mul_f32 v[44:45], v[44:45], v[26:27] op_sel_hi:[1,0]
	global_store_dword v[54:55], v49, off offset:512
	s_nop 1
	v_pk_mul_f32 v[42:43], v[42:43], v[172:173]
	v_pk_mul_f32 v[44:45], v[44:45], v[174:175]
	v_cvt_pk_bf16_f32 v46, v42, v43
	v_mul_f32_e32 v27, 0x42000000, v42
	v_mul_f32_e32 v42, 0x42000000, v43
	v_cvt_pk_bf16_f32 v47, v44, v45
	v_mul_f32_e32 v43, 0x42000000, v44
	v_mul_f32_e32 v44, 0x42000000, v45
	v_med3_f32 v27, v27, s33, v214
	v_med3_f32 v42, v42, s33, v214
	v_mov_b32_e32 v45, v2
	v_cvt_pk_fp8_f32 v45, v27, v42
	v_med3_f32 v43, v43, s33, v214
	v_med3_f32 v44, v44, s33, v214
	global_store_dwordx2 v[28:29], v[46:47], off offset:1536
	s_nop 1
	v_cvt_pk_fp8_f32 v45, v43, v44 op_sel:[0,0,1]
	v_pk_mul_f32 v[38:39], v[38:39], v[26:27] op_sel_hi:[1,0]
	v_pk_mul_f32 v[40:41], v[40:41], v[26:27] op_sel_hi:[1,0]
	global_store_dword v[54:55], v45, off offset:768
	s_nop 1
	v_pk_mul_f32 v[38:39], v[38:39], v[176:177]
	v_pk_mul_f32 v[40:41], v[40:41], v[178:179]
	v_cvt_pk_bf16_f32 v42, v38, v39
	v_mul_f32_e32 v27, 0x42000000, v38
	v_mul_f32_e32 v38, 0x42000000, v39
	v_cvt_pk_bf16_f32 v43, v40, v41
	v_mul_f32_e32 v39, 0x42000000, v40
	v_mul_f32_e32 v40, 0x42000000, v41
	v_med3_f32 v27, v27, s33, v214
	v_med3_f32 v38, v38, s33, v214
	v_mov_b32_e32 v41, v2
	v_cvt_pk_fp8_f32 v41, v27, v38
	v_med3_f32 v39, v39, s33, v214
	v_med3_f32 v40, v40, s33, v214
	global_store_dwordx2 v[28:29], v[42:43], off offset:2048
	s_nop 1
	v_cvt_pk_fp8_f32 v41, v39, v40 op_sel:[0,0,1]
	v_pk_mul_f32 v[34:35], v[34:35], v[26:27] op_sel_hi:[1,0]
	v_pk_mul_f32 v[36:37], v[36:37], v[26:27] op_sel_hi:[1,0]
	global_store_dword v[54:55], v41, off offset:1024
	s_nop 1
	v_pk_mul_f32 v[34:35], v[34:35], v[180:181]
	v_pk_mul_f32 v[36:37], v[36:37], v[182:183]
	v_cvt_pk_bf16_f32 v38, v34, v35
	v_mul_f32_e32 v27, 0x42000000, v34
	v_mul_f32_e32 v34, 0x42000000, v35
	v_cvt_pk_bf16_f32 v39, v36, v37
	v_mul_f32_e32 v35, 0x42000000, v36
	v_mul_f32_e32 v36, 0x42000000, v37
	v_med3_f32 v27, v27, s33, v214
	v_med3_f32 v34, v34, s33, v214
	v_mov_b32_e32 v37, v2
	v_cvt_pk_fp8_f32 v37, v27, v34
	v_med3_f32 v35, v35, s33, v214
	v_med3_f32 v36, v36, s33, v214
	global_store_dwordx2 v[28:29], v[38:39], off offset:2560
	s_nop 1
	v_cvt_pk_fp8_f32 v37, v35, v36 op_sel:[0,0,1]
	v_pk_mul_f32 v[30:31], v[30:31], v[26:27] op_sel_hi:[1,0]
	v_pk_mul_f32 v[32:33], v[32:33], v[26:27] op_sel_hi:[1,0]
	global_store_dword v[54:55], v37, off offset:1280
	s_nop 1
	v_pk_mul_f32 v[30:31], v[30:31], v[184:185]
	v_pk_mul_f32 v[32:33], v[32:33], v[186:187]
	v_cvt_pk_bf16_f32 v34, v30, v31
	v_mul_f32_e32 v27, 0x42000000, v30
	v_mul_f32_e32 v30, 0x42000000, v31
	v_cvt_pk_bf16_f32 v35, v32, v33
	v_mul_f32_e32 v31, 0x42000000, v32
	v_mul_f32_e32 v32, 0x42000000, v33
	v_med3_f32 v27, v27, s33, v214
	v_med3_f32 v30, v30, s33, v214
	v_mov_b32_e32 v33, v2
	v_cvt_pk_fp8_f32 v33, v27, v30
	v_med3_f32 v31, v31, s33, v214
	v_med3_f32 v32, v32, s33, v214
	global_store_dwordx2 v[28:29], v[34:35], off offset:3072
	s_nop 1
	v_cvt_pk_fp8_f32 v33, v31, v32 op_sel:[0,0,1]
	v_pk_mul_f32 v[22:23], v[22:23], v[26:27] op_sel_hi:[1,0]
	v_pk_mul_f32 v[24:25], v[24:25], v[26:27] op_sel_hi:[1,0]
	global_store_dword v[54:55], v33, off offset:1536
	s_nop 1
	v_pk_mul_f32 v[24:25], v[24:25], v[190:191]
	v_pk_mul_f32 v[22:23], v[22:23], v[188:189]
	v_cvt_pk_bf16_f32 v27, v24, v25
	v_cvt_pk_bf16_f32 v26, v22, v23
	v_mul_f32_e32 v22, 0x42000000, v22
	v_mul_f32_e32 v23, 0x42000000, v23
	global_store_dwordx2 v[28:29], v[26:27], off offset:3584
	s_nop 1
	v_med3_f32 v22, v22, s33, v214
	v_med3_f32 v23, v23, s33, v214
	v_mov_b32_e32 v26, v2
	v_cvt_pk_fp8_f32 v26, v22, v23
	v_mul_f32_e32 v24, 0x42000000, v24
	v_mul_f32_e32 v25, 0x42000000, v25
	v_med3_f32 v24, v24, s33, v214
	v_med3_f32 v25, v25, s33, v214
	v_cvt_pk_fp8_f32 v26, v24, v25 op_sel:[0,0,1]
	global_store_dword v[54:55], v26, off offset:1792
	s_nop 1
	s_cbranch_scc0 .LBB0_1326
